# waves 4-7 pre-softmax sleep lengthened from s_sleep 5 to s_sleep 6 on the seam-wait version
# speedup vs baseline: 1.0012x; 1.0012x over previous
.LBB0_517:
	s_or_b64 exec, exec, s[4:5]
	s_lshr_b32 s3, s2, 1
	s_mul_i32 s3, s15, s3
	v_readlane_b32 s4, v255, 16
	s_add_i32 s33, s4, s3
	s_lshl_b32 s3, s33, 7
	s_and_b32 s6, s3, 0xfffff000
	s_lshl_b32 s3, s33, 8
	s_ashr_i32 s82, s33, 3
	s_and_b32 s3, s3, 0x700
	s_and_b32 s2, s2, 1
	s_and_b32 s69, s82, 3
	s_xor_b32 s4, s3, 0xf00
	s_cmp_eq_u32 s2, 0
	s_mov_b32 s2, s6
	s_cselect_b32 s84, s4, s3
	v_writelane_b32 v255, s2, 46
	s_ashr_i32 s7, s6, 31
	s_lshl_b64 s[66:67], s[6:7], 11
	v_writelane_b32 v255, s3, 47
	v_mov_b32_e32 v0, v165
	v_readlane_b32 s2, v255, 25
	s_add_u32 s2, s2, s66
	v_readlane_b32 s3, v255, 26
	s_addc_u32 s3, s3, s67
	s_lshl_b32 s4, s69, 8
	s_add_u32 s6, s2, s4
	s_addc_u32 s7, s3, 0
	s_add_u32 s3, s6, 0x400
	v_writelane_b32 v255, s4, 48
	s_addc_u32 s68, s7, 0
	s_ashr_i32 s83, s82, 31
	s_lshl_b64 s[4:5], s[82:83], 14
	v_readlane_b32 s2, v255, 17
	s_add_u32 s8, s2, s4
	v_readlane_b32 s2, v255, 18
	s_addc_u32 s9, s2, s5
	s_lshl_b32 s4, s82, 6
	s_ashr_i32 s5, s4, 31
	s_lshl_b64 s[4:5], s[4:5], 2
	v_readlane_b32 s2, v255, 21
	s_add_u32 s4, s2, s4
	v_readlane_b32 s2, v255, 22
	s_addc_u32 s5, s2, s5
	v_mov_b32_e32 v3, v161
	v_readfirstlane_b32 s2, v0
	s_ashr_i32 s10, s2, 6
	s_lshl_b32 s12, s10, 5
	s_mov_b32 s2, s12
	v_and_b32_e32 v39, 63, v0
	v_writelane_b32 v255, s2, 49
	s_add_i32 s94, s12, s84
	v_lshlrev_b32_e32 v2, 2, v39
	v_writelane_b32 v255, s3, 50
	s_lshl_b32 s2, s10, 11
	v_lshl_add_u64 v[4:5], s[4:5], 0, v[2:3]
	v_readlane_b32 s11, v255, 28
	s_lshl_b32 s4, s10, 12
	s_ashr_i32 s95, s94, 31
	s_lshl_b32 s78, s10, 3
	flat_load_dword v3, v[4:5]
	s_add_i32 s2, s2, s11
	s_add_i32 s81, s4, s79
	s_lshl_b64 s[12:13], s[94:95], 2
	v_and_b32_e32 v175, 31, v0
	s_add_u32 s4, s8, s12
	v_writelane_b32 v255, s12, 51
	s_addc_u32 s5, s9, s13
	v_lshlrev_b32_e32 v160, 2, v175
	v_lshl_add_u64 v[4:5], s[4:5], 0, v[160:161]
	flat_load_dword v178, v[4:5]
	v_bfe_u32 v4, v0, 4, 2
	v_bitop3_b32 v6, v4, v0, 15 bitop3:0x78
	v_add_u32_e32 v2, s89, v2
	v_writelane_b32 v255, s13, 52
	v_bfe_u32 v176, v0, 5, 1
	v_lshlrev_b32_e32 v6, 4, v6
	v_or_b32_e32 v4, s78, v4
	v_and_b32_e32 v5, 15, v0
	v_lshlrev_b32_e32 v1, 2, v176
	s_mulk_i32 s10, 0x1c00
	v_lshl_or_b32 v170, v4, 11, v6
	v_or_b32_e32 v4, 4, v4
	v_readlane_b32 s4, v255, 33
	v_lshlrev_b32_e32 v40, 4, v39
	v_sub_u32_e32 v7, v175, v1
	v_bitop3_b32 v5, v4, v5, 7 bitop3:0x6c
	v_lshlrev_b32_e32 v4, 11, v4
	s_add_i32 s4, s4, s10
	v_add_u32_e32 v180, s94, v7
	v_lshl_or_b32 v172, v5, 4, v4
	v_add_u32_e32 v181, s4, v40
	v_lshlrev_b32_e32 v174, 4, v176
	s_waitcnt vmcnt(0) lgkmcnt(0)
	ds_write_b32 v2, v3
	s_waitcnt vmcnt(0)
	ds_write_b128 v181, v[128:131]
	ds_write_b128 v181, v[132:135] offset:1024
	ds_write_b128 v181, v[136:139] offset:2048
	ds_write_b128 v181, v[140:143] offset:3072
	ds_write_b128 v181, v[144:147] offset:4096
	ds_write_b128 v181, v[148:151] offset:5120
	ds_write_b128 v181, v[152:155] offset:6144
	s_add_u32 s4, s6, 0x20400
	s_addc_u32 s5, s7, 0
	v_mov_b32_e32 v171, v161
	v_lshl_add_u64 v[2:3], s[4:5], 0, v[170:171]
	s_add_i32 s96, s2, 0x4000
	s_mov_b32 s6, m0
	s_mov_b32 m0, s96
	s_nop 0
	global_load_lds_dwordx4 v[2:3], off
	s_mov_b32 m0, s6
	v_mov_b32_e32 v173, v161
	v_lshl_add_u64 v[2:3], s[4:5], 0, v[172:173]
	s_add_i32 s97, s2, 0x4400
	s_mov_b32 s4, m0
	s_mov_b32 m0, s97
	s_nop 0
	global_load_lds_dwordx4 v[2:3], off
	s_mov_b32 m0, s4
	s_waitcnt lgkmcnt(0)
	s_barrier
	v_lshlrev_b32_e32 v2, 4, v0
	s_movk_i32 s4, 0x70
	v_lshlrev_b32_e32 v34, 8, v175
	v_and_b32_e32 v3, 0x70, v2
	v_bitop3_b32 v35, v174, v2, s4 bitop3:0x78
	s_movk_i32 s4, 0x60
	v_add_u32_e32 v4, s11, v34
	v_bitop3_b32 v36, v174, v3, 32 bitop3:0x36
	v_bitop3_b32 v37, v174, v3, 64 bitop3:0x36
	v_bitop3_b32 v38, v174, v3, s4 bitop3:0x36
	v_add_u32_e32 v182, v35, v4
	v_add_u32_e32 v183, v36, v4
	v_add_u32_e32 v184, v37, v4
	v_add_u32_e32 v185, v38, v4
	ds_read_b128 v[2:5], v182 offset:0
	ds_read_b128 v[6:9], v182 offset:0x2000
	ds_read_b128 v[10:13], v181 offset:0
	ds_read_b128 v[42:45], v183 offset:0
	ds_read_b128 v[46:49], v183 offset:0x2000
	ds_read_b128 v[50:53], v181 offset:0x400
	s_waitcnt lgkmcnt(3)
	s_nop 0
	v_mfma_f32_32x32x16_bf16 v[18:33], v[2:5], v[10:13], 0
	v_mfma_f32_32x32x16_bf16 v[2:17], v[6:9], v[10:13], 0
	ds_read_b128 v[54:57], v184 offset:0
	ds_read_b128 v[58:61], v184 offset:0x2000
	ds_read_b128 v[62:65], v181 offset:0x800
	s_waitcnt lgkmcnt(3)
	v_mfma_f32_32x32x16_bf16 v[18:33], v[42:45], v[50:53], v[18:33]
	v_mfma_f32_32x32x16_bf16 v[2:17], v[46:49], v[50:53], v[2:17]
	ds_read_b128 v[42:45], v185 offset:0
	ds_read_b128 v[46:49], v185 offset:0x2000
	ds_read_b128 v[50:53], v181 offset:0xc00
	s_waitcnt lgkmcnt(3)
	v_mfma_f32_32x32x16_bf16 v[18:33], v[54:57], v[62:65], v[18:33]
	v_mfma_f32_32x32x16_bf16 v[2:17], v[58:61], v[62:65], v[2:17]
	ds_read_b128 v[54:57], v182 offset:0x80
	ds_read_b128 v[58:61], v182 offset:0x2080
	ds_read_b128 v[62:65], v181 offset:0x1000
	s_waitcnt lgkmcnt(3)
	v_mfma_f32_32x32x16_bf16 v[18:33], v[42:45], v[50:53], v[18:33]
	v_mfma_f32_32x32x16_bf16 v[2:17], v[46:49], v[50:53], v[2:17]
	ds_read_b128 v[42:45], v183 offset:0x80
	ds_read_b128 v[46:49], v183 offset:0x2080
	ds_read_b128 v[50:53], v181 offset:0x1400
	s_waitcnt lgkmcnt(3)
	v_mfma_f32_32x32x16_bf16 v[18:33], v[54:57], v[62:65], v[18:33]
	v_mfma_f32_32x32x16_bf16 v[2:17], v[58:61], v[62:65], v[2:17]
	ds_read_b128 v[54:57], v184 offset:0x80
	ds_read_b128 v[58:61], v184 offset:0x2080
	ds_read_b128 v[62:65], v181 offset:0x1800
	s_waitcnt lgkmcnt(3)
	v_mfma_f32_32x32x16_bf16 v[18:33], v[42:45], v[50:53], v[18:33]
	v_mfma_f32_32x32x16_bf16 v[2:17], v[46:49], v[50:53], v[2:17]
	ds_read_b128 v[42:45], v185 offset:0x80
	ds_read_b128 v[46:49], v185 offset:0x2080
	s_waitcnt lgkmcnt(2)
	v_mfma_f32_32x32x16_bf16 v[18:33], v[54:57], v[62:65], v[18:33]
	v_mfma_f32_32x32x16_bf16 v[2:17], v[58:61], v[62:65], v[2:17]
	s_waitcnt lgkmcnt(0)
	v_mfma_f32_32x32x16_bf16 v[18:33], v[42:45], v[166:169], v[18:33]
	v_mfma_f32_32x32x16_bf16 v[2:17], v[46:49], v[166:169], v[2:17]
	s_bitcmp0_b32 s100, 8
	s_cbranch_scc1 .Lstg_a1
	s_waitcnt vmcnt(0)
	s_waitcnt lgkmcnt(0)
	s_barrier
	s_sleep 6

.LBB0_520:
	ds_read_b64_tr_b16 v[144:145], v177 offset:0
	ds_read_b64_tr_b16 v[146:147], v177 offset:0x1000
	ds_read_b64_tr_b16 v[148:149], v177 offset:0x2000
	ds_read_b64_tr_b16 v[150:151], v177 offset:0x3000
	ds_read_b64_tr_b16 v[152:153], v177 offset:0x4000
	ds_read_b64_tr_b16 v[154:155], v177 offset:0x5000
	ds_read_b64_tr_b16 v[156:157], v177 offset:0x6000
	ds_read_b64_tr_b16 v[158:159], v177 offset:0x7000
	s_waitcnt lgkmcnt(6)
	s_nop 0
	v_mfma_f32_32x32x16_bf16 v[112:127], v[144:147], v[128:131], v[112:127]
	ds_read_b64_tr_b16 v[198:199], v177 offset:0x200
	ds_read_b64_tr_b16 v[200:201], v177 offset:0x1200
	s_waitcnt lgkmcnt(6)
	v_mfma_f32_32x32x16_bf16 v[112:127], v[148:151], v[132:135], v[112:127]
	ds_read_b64_tr_b16 v[202:203], v177 offset:0x2200
	ds_read_b64_tr_b16 v[204:205], v177 offset:0x3200
	s_waitcnt lgkmcnt(6)
	v_mfma_f32_32x32x16_bf16 v[112:127], v[152:155], v[136:139], v[112:127]
	ds_read_b64_tr_b16 v[206:207], v177 offset:0x4200
	ds_read_b64_tr_b16 v[208:209], v177 offset:0x5200
	s_waitcnt lgkmcnt(6)
	v_mfma_f32_32x32x16_bf16 v[112:127], v[156:159], v[140:143], v[112:127]
	ds_read_b64_tr_b16 v[210:211], v177 offset:0x6200
	ds_read_b64_tr_b16 v[212:213], v177 offset:0x7200
	s_waitcnt lgkmcnt(6)
	v_mfma_f32_32x32x16_bf16 v[0:15], v[198:201], v[128:131], v[0:15]
	ds_read_b64_tr_b16 v[144:145], v177 offset:0x400
	ds_read_b64_tr_b16 v[146:147], v177 offset:0x1400
	s_waitcnt lgkmcnt(6)
	v_mfma_f32_32x32x16_bf16 v[0:15], v[202:205], v[132:135], v[0:15]
	ds_read_b64_tr_b16 v[148:149], v177 offset:0x2400
	ds_read_b64_tr_b16 v[150:151], v177 offset:0x3400
	s_waitcnt lgkmcnt(6)
	v_mfma_f32_32x32x16_bf16 v[0:15], v[206:209], v[136:139], v[0:15]
	ds_read_b64_tr_b16 v[152:153], v177 offset:0x4400
	ds_read_b64_tr_b16 v[154:155], v177 offset:0x5400
	s_waitcnt lgkmcnt(6)
	v_mfma_f32_32x32x16_bf16 v[0:15], v[210:213], v[140:143], v[0:15]
	ds_read_b64_tr_b16 v[156:157], v177 offset:0x6400
	ds_read_b64_tr_b16 v[158:159], v177 offset:0x7400
	s_waitcnt lgkmcnt(6)
	v_mfma_f32_32x32x16_bf16 v[16:31], v[144:147], v[128:131], v[16:31]
	ds_read_b64_tr_b16 v[198:199], v177 offset:0x600
	ds_read_b64_tr_b16 v[200:201], v177 offset:0x1600
	s_waitcnt lgkmcnt(6)
	v_mfma_f32_32x32x16_bf16 v[16:31], v[148:151], v[132:135], v[16:31]
	ds_read_b64_tr_b16 v[202:203], v177 offset:0x2600
	ds_read_b64_tr_b16 v[204:205], v177 offset:0x3600
	s_waitcnt lgkmcnt(6)
	v_mfma_f32_32x32x16_bf16 v[16:31], v[152:155], v[136:139], v[16:31]
	ds_read_b64_tr_b16 v[206:207], v177 offset:0x4600
	ds_read_b64_tr_b16 v[208:209], v177 offset:0x5600
	s_waitcnt lgkmcnt(6)
	v_mfma_f32_32x32x16_bf16 v[16:31], v[156:159], v[140:143], v[16:31]
	ds_read_b64_tr_b16 v[210:211], v177 offset:0x6600
	ds_read_b64_tr_b16 v[212:213], v177 offset:0x7600
	s_waitcnt lgkmcnt(6)
	v_mfma_f32_32x32x16_bf16 v[32:47], v[198:201], v[128:131], v[32:47]
	ds_read_b64_tr_b16 v[144:145], v177 offset:0x800
	ds_read_b64_tr_b16 v[146:147], v177 offset:0x1800
	s_waitcnt lgkmcnt(6)
	v_mfma_f32_32x32x16_bf16 v[32:47], v[202:205], v[132:135], v[32:47]
	ds_read_b64_tr_b16 v[148:149], v177 offset:0x2800
	ds_read_b64_tr_b16 v[150:151], v177 offset:0x3800
	s_waitcnt lgkmcnt(6)
	v_mfma_f32_32x32x16_bf16 v[32:47], v[206:209], v[136:139], v[32:47]
	ds_read_b64_tr_b16 v[152:153], v177 offset:0x4800
	ds_read_b64_tr_b16 v[154:155], v177 offset:0x5800
	s_waitcnt lgkmcnt(6)
	v_mfma_f32_32x32x16_bf16 v[32:47], v[210:213], v[140:143], v[32:47]
	ds_read_b64_tr_b16 v[156:157], v177 offset:0x6800
	ds_read_b64_tr_b16 v[158:159], v177 offset:0x7800
	s_waitcnt lgkmcnt(6)
	v_mfma_f32_32x32x16_bf16 v[48:63], v[144:147], v[128:131], v[48:63]
	ds_read_b64_tr_b16 v[198:199], v177 offset:0xa00
	ds_read_b64_tr_b16 v[200:201], v177 offset:0x1a00
	s_waitcnt lgkmcnt(6)
	v_mfma_f32_32x32x16_bf16 v[48:63], v[148:151], v[132:135], v[48:63]
	ds_read_b64_tr_b16 v[202:203], v177 offset:0x2a00
	ds_read_b64_tr_b16 v[204:205], v177 offset:0x3a00
	s_waitcnt lgkmcnt(6)
	v_mfma_f32_32x32x16_bf16 v[48:63], v[152:155], v[136:139], v[48:63]
	ds_read_b64_tr_b16 v[206:207], v177 offset:0x4a00
	ds_read_b64_tr_b16 v[208:209], v177 offset:0x5a00
	s_waitcnt lgkmcnt(6)
	v_mfma_f32_32x32x16_bf16 v[48:63], v[156:159], v[140:143], v[48:63]
	ds_read_b64_tr_b16 v[210:211], v177 offset:0x6a00
	ds_read_b64_tr_b16 v[212:213], v177 offset:0x7a00
	s_waitcnt lgkmcnt(6)
	v_mfma_f32_32x32x16_bf16 v[64:79], v[198:201], v[128:131], v[64:79]
	ds_read_b64_tr_b16 v[144:145], v177 offset:0xc00
	ds_read_b64_tr_b16 v[146:147], v177 offset:0x1c00
	s_waitcnt lgkmcnt(6)
	v_mfma_f32_32x32x16_bf16 v[64:79], v[202:205], v[132:135], v[64:79]
	ds_read_b64_tr_b16 v[148:149], v177 offset:0x2c00
	ds_read_b64_tr_b16 v[150:151], v177 offset:0x3c00
	s_waitcnt lgkmcnt(6)
	v_mfma_f32_32x32x16_bf16 v[64:79], v[206:209], v[136:139], v[64:79]
	ds_read_b64_tr_b16 v[152:153], v177 offset:0x4c00
	ds_read_b64_tr_b16 v[154:155], v177 offset:0x5c00
	s_waitcnt lgkmcnt(6)
	v_mfma_f32_32x32x16_bf16 v[64:79], v[210:213], v[140:143], v[64:79]
	ds_read_b64_tr_b16 v[156:157], v177 offset:0x6c00
	ds_read_b64_tr_b16 v[158:159], v177 offset:0x7c00
	s_waitcnt lgkmcnt(6)
	v_mfma_f32_32x32x16_bf16 v[80:95], v[144:147], v[128:131], v[80:95]
	ds_read_b64_tr_b16 v[198:199], v177 offset:0xe00
	ds_read_b64_tr_b16 v[200:201], v177 offset:0x1e00
	s_waitcnt lgkmcnt(6)
	v_mfma_f32_32x32x16_bf16 v[80:95], v[148:151], v[132:135], v[80:95]
	ds_read_b64_tr_b16 v[202:203], v177 offset:0x2e00
	ds_read_b64_tr_b16 v[204:205], v177 offset:0x3e00
	s_waitcnt lgkmcnt(6)
	v_mfma_f32_32x32x16_bf16 v[80:95], v[152:155], v[136:139], v[80:95]
	ds_read_b64_tr_b16 v[206:207], v177 offset:0x4e00
	ds_read_b64_tr_b16 v[208:209], v177 offset:0x5e00
	s_waitcnt lgkmcnt(6)
	v_mfma_f32_32x32x16_bf16 v[80:95], v[156:159], v[140:143], v[80:95]
	ds_read_b64_tr_b16 v[210:211], v177 offset:0x6e00
	ds_read_b64_tr_b16 v[212:213], v177 offset:0x7e00
	s_waitcnt lgkmcnt(6)
	v_mfma_f32_32x32x16_bf16 v[96:111], v[198:201], v[128:131], v[96:111]
	s_waitcnt lgkmcnt(4)
	v_mfma_f32_32x32x16_bf16 v[96:111], v[202:205], v[132:135], v[96:111]
	s_waitcnt lgkmcnt(2)
	v_mfma_f32_32x32x16_bf16 v[96:111], v[206:209], v[136:139], v[96:111]
	s_waitcnt lgkmcnt(0)
	v_mfma_f32_32x32x16_bf16 v[96:111], v[210:213], v[140:143], v[96:111]
	ds_read_b128 v[128:131], v189 offset:0
	ds_read_b128 v[132:135], v189 offset:0x2000
	ds_read_b128 v[136:139], v181 offset:0
	ds_read_b128 v[198:201], v188 offset:0
	ds_read_b128 v[202:205], v188 offset:0x2000
	ds_read_b128 v[206:209], v181 offset:0x400
	s_waitcnt lgkmcnt(3)
	s_nop 0
	v_mfma_f32_32x32x16_bf16 v[144:159], v[128:131], v[136:139], 0
	v_mfma_f32_32x32x16_bf16 v[128:143], v[132:135], v[136:139], 0
	ds_read_b128 v[210:213], v187 offset:0
	ds_read_b128 v[214:217], v187 offset:0x2000
	ds_read_b128 v[218:221], v181 offset:0x800
	s_waitcnt lgkmcnt(3)
	v_mfma_f32_32x32x16_bf16 v[144:159], v[198:201], v[206:209], v[144:159]
	v_mfma_f32_32x32x16_bf16 v[128:143], v[202:205], v[206:209], v[128:143]
	ds_read_b128 v[198:201], v186 offset:0
	ds_read_b128 v[202:205], v186 offset:0x2000
	ds_read_b128 v[206:209], v181 offset:0xc00
	s_waitcnt lgkmcnt(3)
	v_mfma_f32_32x32x16_bf16 v[144:159], v[210:213], v[218:221], v[144:159]
	v_mfma_f32_32x32x16_bf16 v[128:143], v[214:217], v[218:221], v[128:143]
	ds_read_b128 v[210:213], v189 offset:0x80
	ds_read_b128 v[214:217], v189 offset:0x2080
	ds_read_b128 v[218:221], v181 offset:0x1000
	s_waitcnt lgkmcnt(3)
	v_mfma_f32_32x32x16_bf16 v[144:159], v[198:201], v[206:209], v[144:159]
	v_mfma_f32_32x32x16_bf16 v[128:143], v[202:205], v[206:209], v[128:143]
	ds_read_b128 v[198:201], v188 offset:0x80
	ds_read_b128 v[202:205], v188 offset:0x2080
	ds_read_b128 v[206:209], v181 offset:0x1400
	s_waitcnt lgkmcnt(3)
	v_mfma_f32_32x32x16_bf16 v[144:159], v[210:213], v[218:221], v[144:159]
	v_mfma_f32_32x32x16_bf16 v[128:143], v[214:217], v[218:221], v[128:143]
	ds_read_b128 v[210:213], v187 offset:0x80
	ds_read_b128 v[214:217], v187 offset:0x2080
	ds_read_b128 v[218:221], v181 offset:0x1800
	s_waitcnt lgkmcnt(3)
	v_mfma_f32_32x32x16_bf16 v[144:159], v[198:201], v[206:209], v[144:159]
	v_mfma_f32_32x32x16_bf16 v[128:143], v[202:205], v[206:209], v[128:143]
	ds_read_b128 v[198:201], v186 offset:0x80
	ds_read_b128 v[202:205], v186 offset:0x2080
	s_waitcnt lgkmcnt(2)
	v_mfma_f32_32x32x16_bf16 v[144:159], v[210:213], v[218:221], v[144:159]
	v_mfma_f32_32x32x16_bf16 v[128:143], v[214:217], v[218:221], v[128:143]
	s_waitcnt lgkmcnt(0)
	v_mfma_f32_32x32x16_bf16 v[144:159], v[198:201], v[166:169], v[144:159]
	v_mfma_f32_32x32x16_bf16 v[128:143], v[202:205], v[166:169], v[128:143]
	s_bitcmp0_b32 s100, 8
	s_cbranch_scc1 .Lstg_a2
	s_waitcnt vmcnt(0)
	s_waitcnt lgkmcnt(0)
	s_barrier
	s_sleep 6

.LBB0_526:
	s_add_u32 s33, s72, s84
	s_addc_u32 s92, s73, s90
	s_add_u32 s4, s33, 0x2dd40800
	s_addc_u32 s5, s92, 0
	s_mov_b32 m0, s81
	s_nop 0
	global_load_lds_dwordx4 v162, s[4:5]
	s_add_i32 m0, s78, 0xffffff80
	s_nop 0
	global_load_lds_dwordx4 v162, s[4:5] offset:128
	s_add_i32 m0, s69, 0xffffff00
	s_nop 0
	global_load_lds_dwordx4 v162, s[4:5] offset:256
	s_add_i32 m0, s68, 0xfffffe80
	s_nop 0
	global_load_lds_dwordx4 v162, s[4:5] offset:384
	ds_read_b64_tr_b16 v[144:145], v177 offset:0x8000
	ds_read_b64_tr_b16 v[146:147], v177 offset:0x9000
	ds_read_b64_tr_b16 v[148:149], v177 offset:0xa000
	ds_read_b64_tr_b16 v[150:151], v177 offset:0xb000
	ds_read_b64_tr_b16 v[152:153], v177 offset:0xc000
	ds_read_b64_tr_b16 v[154:155], v177 offset:0xd000
	ds_read_b64_tr_b16 v[156:157], v177 offset:0xe000
	ds_read_b64_tr_b16 v[158:159], v177 offset:0xf000
	s_waitcnt lgkmcnt(6)
	s_nop 1
	v_mfma_f32_32x32x16_bf16 v[112:127], v[144:147], v[128:131], v[112:127]
	ds_read_b64_tr_b16 v[236:237], v177 offset:0x8200
	ds_read_b64_tr_b16 v[238:239], v177 offset:0x9200
	s_waitcnt lgkmcnt(6)
	v_mfma_f32_32x32x16_bf16 v[112:127], v[148:151], v[132:135], v[112:127]
	ds_read_b64_tr_b16 v[240:241], v177 offset:0xa200
	ds_read_b64_tr_b16 v[242:243], v177 offset:0xb200
	s_waitcnt lgkmcnt(6)
	v_mfma_f32_32x32x16_bf16 v[112:127], v[152:155], v[136:139], v[112:127]
	ds_read_b64_tr_b16 v[244:245], v177 offset:0xc200
	ds_read_b64_tr_b16 v[246:247], v177 offset:0xd200
	s_waitcnt lgkmcnt(6)
	v_mfma_f32_32x32x16_bf16 v[112:127], v[156:159], v[140:143], v[112:127]
	ds_read_b64_tr_b16 v[248:249], v177 offset:0xe200
	ds_read_b64_tr_b16 v[250:251], v177 offset:0xf200
	s_waitcnt lgkmcnt(6)
	v_mfma_f32_32x32x16_bf16 v[0:15], v[236:239], v[128:131], v[0:15]
	ds_read_b64_tr_b16 v[144:145], v177 offset:0x8400
	ds_read_b64_tr_b16 v[146:147], v177 offset:0x9400
	s_waitcnt lgkmcnt(6)
	v_mfma_f32_32x32x16_bf16 v[0:15], v[240:243], v[132:135], v[0:15]
	ds_read_b64_tr_b16 v[148:149], v177 offset:0xa400
	ds_read_b64_tr_b16 v[150:151], v177 offset:0xb400
	s_waitcnt lgkmcnt(6)
	v_mfma_f32_32x32x16_bf16 v[0:15], v[244:247], v[136:139], v[0:15]
	ds_read_b64_tr_b16 v[152:153], v177 offset:0xc400
	ds_read_b64_tr_b16 v[154:155], v177 offset:0xd400
	s_waitcnt lgkmcnt(6)
	v_mfma_f32_32x32x16_bf16 v[0:15], v[248:251], v[140:143], v[0:15]
	ds_read_b64_tr_b16 v[156:157], v177 offset:0xe400
	ds_read_b64_tr_b16 v[158:159], v177 offset:0xf400
	s_waitcnt lgkmcnt(6)
	v_mfma_f32_32x32x16_bf16 v[16:31], v[144:147], v[128:131], v[16:31]
	ds_read_b64_tr_b16 v[236:237], v177 offset:0x8600
	ds_read_b64_tr_b16 v[238:239], v177 offset:0x9600
	s_waitcnt lgkmcnt(6)
	v_mfma_f32_32x32x16_bf16 v[16:31], v[148:151], v[132:135], v[16:31]
	ds_read_b64_tr_b16 v[240:241], v177 offset:0xa600
	ds_read_b64_tr_b16 v[242:243], v177 offset:0xb600
	s_waitcnt lgkmcnt(6)
	v_mfma_f32_32x32x16_bf16 v[16:31], v[152:155], v[136:139], v[16:31]
	ds_read_b64_tr_b16 v[244:245], v177 offset:0xc600
	ds_read_b64_tr_b16 v[246:247], v177 offset:0xd600
	s_waitcnt lgkmcnt(6)
	v_mfma_f32_32x32x16_bf16 v[16:31], v[156:159], v[140:143], v[16:31]
	ds_read_b64_tr_b16 v[248:249], v177 offset:0xe600
	ds_read_b64_tr_b16 v[250:251], v177 offset:0xf600
	s_waitcnt lgkmcnt(6)
	v_mfma_f32_32x32x16_bf16 v[32:47], v[236:239], v[128:131], v[32:47]
	ds_read_b64_tr_b16 v[144:145], v177 offset:0x8800
	ds_read_b64_tr_b16 v[146:147], v177 offset:0x9800
	s_waitcnt lgkmcnt(6)
	v_mfma_f32_32x32x16_bf16 v[32:47], v[240:243], v[132:135], v[32:47]
	ds_read_b64_tr_b16 v[148:149], v177 offset:0xa800
	ds_read_b64_tr_b16 v[150:151], v177 offset:0xb800
	s_waitcnt lgkmcnt(6)
	v_mfma_f32_32x32x16_bf16 v[32:47], v[244:247], v[136:139], v[32:47]
	ds_read_b64_tr_b16 v[152:153], v177 offset:0xc800
	ds_read_b64_tr_b16 v[154:155], v177 offset:0xd800
	s_waitcnt lgkmcnt(6)
	v_mfma_f32_32x32x16_bf16 v[32:47], v[248:251], v[140:143], v[32:47]
	ds_read_b64_tr_b16 v[156:157], v177 offset:0xe800
	ds_read_b64_tr_b16 v[158:159], v177 offset:0xf800
	s_waitcnt lgkmcnt(6)
	v_mfma_f32_32x32x16_bf16 v[48:63], v[144:147], v[128:131], v[48:63]
	ds_read_b64_tr_b16 v[236:237], v177 offset:0x8a00
	ds_read_b64_tr_b16 v[238:239], v177 offset:0x9a00
	s_waitcnt lgkmcnt(6)
	v_mfma_f32_32x32x16_bf16 v[48:63], v[148:151], v[132:135], v[48:63]
	ds_read_b64_tr_b16 v[240:241], v177 offset:0xaa00
	ds_read_b64_tr_b16 v[242:243], v177 offset:0xba00
	s_waitcnt lgkmcnt(6)
	v_mfma_f32_32x32x16_bf16 v[48:63], v[152:155], v[136:139], v[48:63]
	ds_read_b64_tr_b16 v[244:245], v177 offset:0xca00
	ds_read_b64_tr_b16 v[246:247], v177 offset:0xda00
	s_waitcnt lgkmcnt(6)
	v_mfma_f32_32x32x16_bf16 v[48:63], v[156:159], v[140:143], v[48:63]
	ds_read_b64_tr_b16 v[248:249], v177 offset:0xea00
	ds_read_b64_tr_b16 v[250:251], v177 offset:0xfa00
	s_waitcnt lgkmcnt(6)
	v_mfma_f32_32x32x16_bf16 v[64:79], v[236:239], v[128:131], v[64:79]
	ds_read_b64_tr_b16 v[144:145], v177 offset:0x8c00
	ds_read_b64_tr_b16 v[146:147], v177 offset:0x9c00
	s_waitcnt lgkmcnt(6)
	v_mfma_f32_32x32x16_bf16 v[64:79], v[240:243], v[132:135], v[64:79]
	ds_read_b64_tr_b16 v[148:149], v177 offset:0xac00
	ds_read_b64_tr_b16 v[150:151], v177 offset:0xbc00
	s_waitcnt lgkmcnt(6)
	v_mfma_f32_32x32x16_bf16 v[64:79], v[244:247], v[136:139], v[64:79]
	ds_read_b64_tr_b16 v[152:153], v177 offset:0xcc00
	ds_read_b64_tr_b16 v[154:155], v177 offset:0xdc00
	s_waitcnt lgkmcnt(6)
	v_mfma_f32_32x32x16_bf16 v[64:79], v[248:251], v[140:143], v[64:79]
	ds_read_b64_tr_b16 v[156:157], v177 offset:0xec00
	ds_read_b64_tr_b16 v[158:159], v177 offset:0xfc00
	s_waitcnt lgkmcnt(6)
	v_mfma_f32_32x32x16_bf16 v[80:95], v[144:147], v[128:131], v[80:95]
	ds_read_b64_tr_b16 v[236:237], v177 offset:0x8e00
	ds_read_b64_tr_b16 v[238:239], v177 offset:0x9e00
	s_waitcnt lgkmcnt(6)
	v_mfma_f32_32x32x16_bf16 v[80:95], v[148:151], v[132:135], v[80:95]
	ds_read_b64_tr_b16 v[240:241], v177 offset:0xae00
	ds_read_b64_tr_b16 v[242:243], v177 offset:0xbe00
	s_waitcnt lgkmcnt(6)
	v_mfma_f32_32x32x16_bf16 v[80:95], v[152:155], v[136:139], v[80:95]
	ds_read_b64_tr_b16 v[244:245], v177 offset:0xce00
	ds_read_b64_tr_b16 v[246:247], v177 offset:0xde00
	s_waitcnt lgkmcnt(6)
	v_mfma_f32_32x32x16_bf16 v[80:95], v[156:159], v[140:143], v[80:95]
	ds_read_b64_tr_b16 v[248:249], v177 offset:0xee00
	ds_read_b64_tr_b16 v[250:251], v177 offset:0xfe00
	s_waitcnt lgkmcnt(6)
	v_mfma_f32_32x32x16_bf16 v[96:111], v[236:239], v[128:131], v[96:111]
	s_waitcnt lgkmcnt(4)
	v_mfma_f32_32x32x16_bf16 v[96:111], v[240:243], v[132:135], v[96:111]
	s_waitcnt lgkmcnt(2)
	v_mfma_f32_32x32x16_bf16 v[96:111], v[244:247], v[136:139], v[96:111]
	s_waitcnt lgkmcnt(0)
	v_mfma_f32_32x32x16_bf16 v[96:111], v[248:251], v[140:143], v[96:111]
	ds_read_b128 v[128:131], v182 offset:0
	ds_read_b128 v[132:135], v182 offset:0x2000
	ds_read_b128 v[136:139], v181 offset:0
	ds_read_b128 v[236:239], v183 offset:0
	ds_read_b128 v[240:243], v183 offset:0x2000
	ds_read_b128 v[244:247], v181 offset:0x400
	s_waitcnt lgkmcnt(3)
	s_nop 0
	v_mfma_f32_32x32x16_bf16 v[144:159], v[128:131], v[136:139], 0
	v_mfma_f32_32x32x16_bf16 v[128:143], v[132:135], v[136:139], 0
	ds_read_b128 v[248:251], v184 offset:0
	ds_read_b128 v[194:197], v184 offset:0x2000
	ds_read_b128 v[222:225], v181 offset:0x800
	s_waitcnt lgkmcnt(3)
	v_mfma_f32_32x32x16_bf16 v[144:159], v[236:239], v[244:247], v[144:159]
	v_mfma_f32_32x32x16_bf16 v[128:143], v[240:243], v[244:247], v[128:143]
	ds_read_b128 v[236:239], v185 offset:0
	ds_read_b128 v[240:243], v185 offset:0x2000
	ds_read_b128 v[244:247], v181 offset:0xc00
	s_waitcnt lgkmcnt(3)
	v_mfma_f32_32x32x16_bf16 v[144:159], v[248:251], v[222:225], v[144:159]
	v_mfma_f32_32x32x16_bf16 v[128:143], v[194:197], v[222:225], v[128:143]
	ds_read_b128 v[194:197], v182 offset:0x80
	ds_read_b128 v[222:225], v182 offset:0x2080
	ds_read_b128 v[248:251], v181 offset:0x1000
	s_waitcnt lgkmcnt(3)
	v_mfma_f32_32x32x16_bf16 v[144:159], v[236:239], v[244:247], v[144:159]
	v_mfma_f32_32x32x16_bf16 v[128:143], v[240:243], v[244:247], v[128:143]
	ds_read_b128 v[236:239], v183 offset:0x80
	ds_read_b128 v[240:243], v183 offset:0x2080
	ds_read_b128 v[244:247], v181 offset:0x1400
	s_waitcnt lgkmcnt(3)
	v_mfma_f32_32x32x16_bf16 v[144:159], v[194:197], v[248:251], v[144:159]
	v_mfma_f32_32x32x16_bf16 v[128:143], v[222:225], v[248:251], v[128:143]
	ds_read_b128 v[194:197], v184 offset:0x80
	ds_read_b128 v[222:225], v184 offset:0x2080
	ds_read_b128 v[248:251], v181 offset:0x1800
	s_waitcnt lgkmcnt(3)
	v_mfma_f32_32x32x16_bf16 v[144:159], v[236:239], v[244:247], v[144:159]
	v_mfma_f32_32x32x16_bf16 v[128:143], v[240:243], v[244:247], v[128:143]
	ds_read_b128 v[236:239], v185 offset:0x80
	ds_read_b128 v[240:243], v185 offset:0x2080
	s_waitcnt lgkmcnt(2)
	v_mfma_f32_32x32x16_bf16 v[144:159], v[194:197], v[248:251], v[144:159]
	v_mfma_f32_32x32x16_bf16 v[128:143], v[222:225], v[248:251], v[128:143]
	s_waitcnt lgkmcnt(0)
	v_mfma_f32_32x32x16_bf16 v[144:159], v[236:239], v[166:169], v[144:159]
	v_mfma_f32_32x32x16_bf16 v[128:143], v[240:243], v[166:169], v[128:143]
	s_bitcmp0_b32 s100, 8
	s_cbranch_scc1 .Lstg_a3
	s_waitcnt vmcnt(0)
	s_waitcnt lgkmcnt(0)
	s_barrier
	s_sleep 6

.LBB0_539:
	ds_read_b64_tr_b16 v[144:145], v177 offset:0
	ds_read_b64_tr_b16 v[146:147], v177 offset:0x1000
	ds_read_b64_tr_b16 v[148:149], v177 offset:0x2000
	ds_read_b64_tr_b16 v[150:151], v177 offset:0x3000
	ds_read_b64_tr_b16 v[152:153], v177 offset:0x4000
	ds_read_b64_tr_b16 v[154:155], v177 offset:0x5000
	ds_read_b64_tr_b16 v[156:157], v177 offset:0x6000
	ds_read_b64_tr_b16 v[158:159], v177 offset:0x7000
	s_waitcnt lgkmcnt(6)
	s_nop 0
	v_mfma_f32_32x32x16_bf16 v[112:127], v[144:147], v[128:131], v[112:127]
	ds_read_b64_tr_b16 v[170:171], v177 offset:0x200
	ds_read_b64_tr_b16 v[172:173], v177 offset:0x1200
	s_waitcnt lgkmcnt(6)
	v_mfma_f32_32x32x16_bf16 v[112:127], v[148:151], v[132:135], v[112:127]
	ds_read_b64_tr_b16 v[182:183], v177 offset:0x2200
	ds_read_b64_tr_b16 v[184:185], v177 offset:0x3200
	s_waitcnt lgkmcnt(6)
	v_mfma_f32_32x32x16_bf16 v[112:127], v[152:155], v[136:139], v[112:127]
	ds_read_b64_tr_b16 v[190:191], v177 offset:0x4200
	ds_read_b64_tr_b16 v[192:193], v177 offset:0x5200
	s_waitcnt lgkmcnt(6)
	v_mfma_f32_32x32x16_bf16 v[112:127], v[156:159], v[140:143], v[112:127]
	ds_read_b64_tr_b16 v[198:199], v177 offset:0x6200
	ds_read_b64_tr_b16 v[200:201], v177 offset:0x7200
	s_waitcnt lgkmcnt(6)
	v_mfma_f32_32x32x16_bf16 v[0:15], v[170:173], v[128:131], v[0:15]
	ds_read_b64_tr_b16 v[144:145], v177 offset:0x400
	ds_read_b64_tr_b16 v[146:147], v177 offset:0x1400
	s_waitcnt lgkmcnt(6)
	v_mfma_f32_32x32x16_bf16 v[0:15], v[182:185], v[132:135], v[0:15]
	ds_read_b64_tr_b16 v[148:149], v177 offset:0x2400
	ds_read_b64_tr_b16 v[150:151], v177 offset:0x3400
	s_waitcnt lgkmcnt(6)
	v_mfma_f32_32x32x16_bf16 v[0:15], v[190:193], v[136:139], v[0:15]
	ds_read_b64_tr_b16 v[152:153], v177 offset:0x4400
	ds_read_b64_tr_b16 v[154:155], v177 offset:0x5400
	s_waitcnt lgkmcnt(6)
	v_mfma_f32_32x32x16_bf16 v[0:15], v[198:201], v[140:143], v[0:15]
	ds_read_b64_tr_b16 v[156:157], v177 offset:0x6400
	ds_read_b64_tr_b16 v[158:159], v177 offset:0x7400
	s_waitcnt lgkmcnt(6)
	v_mfma_f32_32x32x16_bf16 v[16:31], v[144:147], v[128:131], v[16:31]
	ds_read_b64_tr_b16 v[170:171], v177 offset:0x600
	ds_read_b64_tr_b16 v[172:173], v177 offset:0x1600
	s_waitcnt lgkmcnt(6)
	v_mfma_f32_32x32x16_bf16 v[16:31], v[148:151], v[132:135], v[16:31]
	ds_read_b64_tr_b16 v[182:183], v177 offset:0x2600
	ds_read_b64_tr_b16 v[184:185], v177 offset:0x3600
	s_waitcnt lgkmcnt(6)
	v_mfma_f32_32x32x16_bf16 v[16:31], v[152:155], v[136:139], v[16:31]
	ds_read_b64_tr_b16 v[190:191], v177 offset:0x4600
	ds_read_b64_tr_b16 v[192:193], v177 offset:0x5600
	s_waitcnt lgkmcnt(6)
	v_mfma_f32_32x32x16_bf16 v[16:31], v[156:159], v[140:143], v[16:31]
	ds_read_b64_tr_b16 v[198:199], v177 offset:0x6600
	ds_read_b64_tr_b16 v[200:201], v177 offset:0x7600
	s_waitcnt lgkmcnt(6)
	v_mfma_f32_32x32x16_bf16 v[32:47], v[170:173], v[128:131], v[32:47]
	ds_read_b64_tr_b16 v[144:145], v177 offset:0x800
	ds_read_b64_tr_b16 v[146:147], v177 offset:0x1800
	s_waitcnt lgkmcnt(6)
	v_mfma_f32_32x32x16_bf16 v[32:47], v[182:185], v[132:135], v[32:47]
	ds_read_b64_tr_b16 v[148:149], v177 offset:0x2800
	ds_read_b64_tr_b16 v[150:151], v177 offset:0x3800
	s_waitcnt lgkmcnt(6)
	v_mfma_f32_32x32x16_bf16 v[32:47], v[190:193], v[136:139], v[32:47]
	ds_read_b64_tr_b16 v[152:153], v177 offset:0x4800
	ds_read_b64_tr_b16 v[154:155], v177 offset:0x5800
	s_waitcnt lgkmcnt(6)
	v_mfma_f32_32x32x16_bf16 v[32:47], v[198:201], v[140:143], v[32:47]
	ds_read_b64_tr_b16 v[156:157], v177 offset:0x6800
	ds_read_b64_tr_b16 v[158:159], v177 offset:0x7800
	s_waitcnt lgkmcnt(6)
	v_mfma_f32_32x32x16_bf16 v[48:63], v[144:147], v[128:131], v[48:63]
	ds_read_b64_tr_b16 v[170:171], v177 offset:0xa00
	ds_read_b64_tr_b16 v[172:173], v177 offset:0x1a00
	s_waitcnt lgkmcnt(6)
	v_mfma_f32_32x32x16_bf16 v[48:63], v[148:151], v[132:135], v[48:63]
	ds_read_b64_tr_b16 v[182:183], v177 offset:0x2a00
	ds_read_b64_tr_b16 v[184:185], v177 offset:0x3a00
	s_waitcnt lgkmcnt(6)
	v_mfma_f32_32x32x16_bf16 v[48:63], v[152:155], v[136:139], v[48:63]
	ds_read_b64_tr_b16 v[190:191], v177 offset:0x4a00
	ds_read_b64_tr_b16 v[192:193], v177 offset:0x5a00
	s_waitcnt lgkmcnt(6)
	v_mfma_f32_32x32x16_bf16 v[48:63], v[156:159], v[140:143], v[48:63]
	ds_read_b64_tr_b16 v[198:199], v177 offset:0x6a00
	ds_read_b64_tr_b16 v[200:201], v177 offset:0x7a00
	s_waitcnt lgkmcnt(6)
	v_mfma_f32_32x32x16_bf16 v[64:79], v[170:173], v[128:131], v[64:79]
	ds_read_b64_tr_b16 v[144:145], v177 offset:0xc00
	ds_read_b64_tr_b16 v[146:147], v177 offset:0x1c00
	s_waitcnt lgkmcnt(6)
	v_mfma_f32_32x32x16_bf16 v[64:79], v[182:185], v[132:135], v[64:79]
	ds_read_b64_tr_b16 v[148:149], v177 offset:0x2c00
	ds_read_b64_tr_b16 v[150:151], v177 offset:0x3c00
	s_waitcnt lgkmcnt(6)
	v_mfma_f32_32x32x16_bf16 v[64:79], v[190:193], v[136:139], v[64:79]
	ds_read_b64_tr_b16 v[152:153], v177 offset:0x4c00
	ds_read_b64_tr_b16 v[154:155], v177 offset:0x5c00
	s_waitcnt lgkmcnt(6)
	v_mfma_f32_32x32x16_bf16 v[64:79], v[198:201], v[140:143], v[64:79]
	ds_read_b64_tr_b16 v[156:157], v177 offset:0x6c00
	ds_read_b64_tr_b16 v[158:159], v177 offset:0x7c00
	s_waitcnt lgkmcnt(6)
	v_mfma_f32_32x32x16_bf16 v[80:95], v[144:147], v[128:131], v[80:95]
	ds_read_b64_tr_b16 v[170:171], v177 offset:0xe00
	ds_read_b64_tr_b16 v[172:173], v177 offset:0x1e00
	s_waitcnt lgkmcnt(6)
	v_mfma_f32_32x32x16_bf16 v[80:95], v[148:151], v[132:135], v[80:95]
	ds_read_b64_tr_b16 v[182:183], v177 offset:0x2e00
	ds_read_b64_tr_b16 v[184:185], v177 offset:0x3e00
	s_waitcnt lgkmcnt(6)
	v_mfma_f32_32x32x16_bf16 v[80:95], v[152:155], v[136:139], v[80:95]
	ds_read_b64_tr_b16 v[190:191], v177 offset:0x4e00
	ds_read_b64_tr_b16 v[192:193], v177 offset:0x5e00
	s_waitcnt lgkmcnt(6)
	v_mfma_f32_32x32x16_bf16 v[80:95], v[156:159], v[140:143], v[80:95]
	ds_read_b64_tr_b16 v[198:199], v177 offset:0x6e00
	ds_read_b64_tr_b16 v[200:201], v177 offset:0x7e00
	s_waitcnt lgkmcnt(6)
	v_mfma_f32_32x32x16_bf16 v[96:111], v[170:173], v[128:131], v[96:111]
	s_waitcnt lgkmcnt(4)
	v_mfma_f32_32x32x16_bf16 v[96:111], v[182:185], v[132:135], v[96:111]
	s_waitcnt lgkmcnt(2)
	v_mfma_f32_32x32x16_bf16 v[96:111], v[190:193], v[136:139], v[96:111]
	s_waitcnt lgkmcnt(0)
	v_mfma_f32_32x32x16_bf16 v[96:111], v[198:201], v[140:143], v[96:111]
	ds_read_b128 v[128:131], v189 offset:0
	ds_read_b128 v[132:135], v189 offset:0x2000
	ds_read_b128 v[136:139], v181 offset:0
	ds_read_b128 v[170:173], v188 offset:0
	ds_read_b128 v[182:185], v188 offset:0x2000
	ds_read_b128 v[190:193], v181 offset:0x400
	s_waitcnt lgkmcnt(3)
	s_nop 0
	v_mfma_f32_32x32x16_bf16 v[144:159], v[128:131], v[136:139], 0
	v_mfma_f32_32x32x16_bf16 v[128:143], v[132:135], v[136:139], 0
	ds_read_b128 v[198:201], v187 offset:0
	ds_read_b128 v[202:205], v187 offset:0x2000
	ds_read_b128 v[206:209], v181 offset:0x800
	s_waitcnt lgkmcnt(3)
	v_mfma_f32_32x32x16_bf16 v[144:159], v[170:173], v[190:193], v[144:159]
	v_mfma_f32_32x32x16_bf16 v[128:143], v[182:185], v[190:193], v[128:143]
	ds_read_b128 v[170:173], v186 offset:0
	ds_read_b128 v[182:185], v186 offset:0x2000
	ds_read_b128 v[190:193], v181 offset:0xc00
	s_waitcnt lgkmcnt(3)
	v_mfma_f32_32x32x16_bf16 v[144:159], v[198:201], v[206:209], v[144:159]
	v_mfma_f32_32x32x16_bf16 v[128:143], v[202:205], v[206:209], v[128:143]
	ds_read_b128 v[198:201], v189 offset:0x80
	ds_read_b128 v[202:205], v189 offset:0x2080
	ds_read_b128 v[206:209], v181 offset:0x1000
	s_waitcnt lgkmcnt(3)
	v_mfma_f32_32x32x16_bf16 v[144:159], v[170:173], v[190:193], v[144:159]
	v_mfma_f32_32x32x16_bf16 v[128:143], v[182:185], v[190:193], v[128:143]
	ds_read_b128 v[170:173], v188 offset:0x80
	ds_read_b128 v[182:185], v188 offset:0x2080
	ds_read_b128 v[188:191], v181 offset:0x1400
	s_waitcnt lgkmcnt(3)
	v_mfma_f32_32x32x16_bf16 v[144:159], v[198:201], v[206:209], v[144:159]
	v_mfma_f32_32x32x16_bf16 v[128:143], v[202:205], v[206:209], v[128:143]
	ds_read_b128 v[198:201], v187 offset:0x80
	ds_read_b128 v[202:205], v187 offset:0x2080
	ds_read_b128 v[206:209], v181 offset:0x1800
	s_waitcnt lgkmcnt(3)
	v_mfma_f32_32x32x16_bf16 v[144:159], v[170:173], v[188:191], v[144:159]
	v_mfma_f32_32x32x16_bf16 v[128:143], v[182:185], v[188:191], v[128:143]
	ds_read_b128 v[170:173], v186 offset:0x80
	ds_read_b128 v[182:185], v186 offset:0x2080
	s_waitcnt lgkmcnt(2)
	v_mfma_f32_32x32x16_bf16 v[144:159], v[198:201], v[206:209], v[144:159]
	v_mfma_f32_32x32x16_bf16 v[128:143], v[202:205], v[206:209], v[128:143]
	s_waitcnt lgkmcnt(0)
	v_mfma_f32_32x32x16_bf16 v[144:159], v[170:173], v[166:169], v[144:159]
	v_mfma_f32_32x32x16_bf16 v[128:143], v[182:185], v[166:169], v[128:143]
	s_bitcmp0_b32 s100, 8
	s_cbranch_scc1 .Lstg_a4
	s_waitcnt vmcnt(0)
	s_waitcnt lgkmcnt(0)
	s_barrier
	s_sleep 6

.LBB0_554:
	s_or_b64 exec, exec, s[4:5]
	s_ashr_i32 s95, s94, 31
	s_add_u32 s4, s2, s16
	s_addc_u32 s3, s3, 0
	v_mov_b32_e32 v38, v165
	s_add_u32 s2, s4, 0x2800
	s_addc_u32 s33, s3, 0
	v_readfirstlane_b32 s5, v38
	s_ashr_i32 s79, s5, 6
	v_bfe_u32 v0, v38, 5, 1
	v_and_b32_e32 v175, 31, v38
	s_lshl_b32 s92, s79, 5
	v_lshlrev_b32_e32 v32, 2, v0
	s_add_i32 s82, s92, s78
	v_sub_u32_e32 v1, v175, v32
	v_lshlrev_b32_e32 v176, 4, v0
	s_lshl_b32 s76, s79, 3
	v_bfe_u32 v0, v38, 4, 2
	v_writelane_b32 v255, s16, 17
	v_add_u32_e32 v179, s82, v1
	v_or_b32_e32 v1, s76, v0
	v_and_b32_e32 v2, 15, v38
	s_lshl_b32 s5, s79, 12
	v_and_b32_e32 v39, 63, v38
	v_bitop3_b32 v3, v0, v38, 15 bitop3:0x78
	v_mul_lo_u32 v1, v1, s84
	v_bitop3_b32 v0, v0, v2, 4 bitop3:0x36
	s_add_i32 s93, s5, s77
	s_mul_i32 s5, s79, 0x1c00
	v_readlane_b32 s7, v255, 51
	s_waitcnt vmcnt(16)
	v_lshlrev_b32_e32 v40, 4, v39
	v_lshl_or_b32 v0, v0, 4, v1
	s_lshl_b32 s83, s79, 11
	v_readlane_b32 s6, v255, 53
	s_add_i32 s5, s7, s5
	v_lshl_or_b32 v160, v3, 4, v1
	v_add_u32_e32 v170, 0x1a000, v0
	s_add_i32 s83, s83, s6
	v_add_u32_e32 v180, s5, v40
	s_waitcnt vmcnt(16) lgkmcnt(0)
	v_mov_b64_e32 v[218:219], v[128:129]
	v_mov_b64_e32 v[220:221], v[130:131]
	v_mov_b64_e32 v[222:223], v[132:133]
	v_mov_b64_e32 v[224:225], v[134:135]
	v_mov_b64_e32 v[230:231], v[136:137]
	v_mov_b64_e32 v[232:233], v[138:139]
	v_mov_b64_e32 v[234:235], v[140:141]
	v_mov_b64_e32 v[236:237], v[142:143]
	v_mov_b64_e32 v[238:239], v[144:145]
	v_mov_b64_e32 v[240:241], v[146:147]
	v_mov_b64_e32 v[242:243], v[148:149]
	v_mov_b64_e32 v[244:245], v[150:151]
	v_mov_b64_e32 v[246:247], v[152:153]
	v_mov_b64_e32 v[248:249], v[154:155]
	s_add_u32 s4, s4, 0x1a2800
	s_addc_u32 s5, s3, 0
	v_lshl_add_u64 v[0:1], s[4:5], 0, v[160:161]
	s_add_i32 s84, s83, 0x4000
	s_mov_b32 s3, m0
	s_mov_b32 m0, s84
	s_nop 0
	global_load_lds_dwordx4 v[0:1], off
	s_mov_b32 m0, s3
	v_mov_b32_e32 v171, v161
	v_lshl_add_u64 v[0:1], s[4:5], 0, v[170:171]
	s_add_i32 s85, s83, 0x4400
	s_mov_b32 s3, m0
	s_mov_b32 m0, s85
	s_nop 0
	global_load_lds_dwordx4 v[0:1], off
	s_mov_b32 m0, s3
	s_waitcnt lgkmcnt(0)
	s_barrier
	v_lshlrev_b32_e32 v0, 4, v38
	s_movk_i32 s3, 0x70
	v_lshlrev_b32_e32 v33, 8, v175
	v_and_b32_e32 v1, 0x70, v0
	v_bitop3_b32 v34, v176, v0, s3 bitop3:0x78
	s_movk_i32 s3, 0x60
	v_add_u32_e32 v2, s6, v33
	v_bitop3_b32 v35, v176, v1, 32 bitop3:0x36
	v_bitop3_b32 v36, v176, v1, 64 bitop3:0x36
	v_bitop3_b32 v37, v176, v1, s3 bitop3:0x36
	v_add_u32_e32 v181, v34, v2
	v_add_u32_e32 v182, v35, v2
	v_add_u32_e32 v183, v36, v2
	v_add_u32_e32 v184, v37, v2
	ds_read_b128 v[0:3], v181 offset:0
	ds_read_b128 v[4:7], v181 offset:0x2000
	ds_read_b128 v[42:45], v182 offset:0
	ds_read_b128 v[46:49], v182 offset:0x2000
	s_waitcnt lgkmcnt(2)
	s_nop 0
	v_mfma_f32_32x32x16_bf16 v[16:31], v[0:3], v[218:221], 0
	v_mfma_f32_32x32x16_bf16 v[0:15], v[4:7], v[218:221], 0
	ds_read_b128 v[54:57], v183 offset:0
	ds_read_b128 v[58:61], v183 offset:0x2000
	s_waitcnt lgkmcnt(2)
	v_mfma_f32_32x32x16_bf16 v[16:31], v[42:45], v[222:225], v[16:31]
	v_mfma_f32_32x32x16_bf16 v[0:15], v[46:49], v[222:225], v[0:15]
	ds_read_b128 v[42:45], v184 offset:0
	ds_read_b128 v[46:49], v184 offset:0x2000
	s_waitcnt lgkmcnt(2)
	v_mfma_f32_32x32x16_bf16 v[16:31], v[54:57], v[230:233], v[16:31]
	v_mfma_f32_32x32x16_bf16 v[0:15], v[58:61], v[230:233], v[0:15]
	ds_read_b128 v[54:57], v181 offset:0x80
	ds_read_b128 v[58:61], v181 offset:0x2080
	s_waitcnt lgkmcnt(2)
	v_mfma_f32_32x32x16_bf16 v[16:31], v[42:45], v[234:237], v[16:31]
	v_mfma_f32_32x32x16_bf16 v[0:15], v[46:49], v[234:237], v[0:15]
	ds_read_b128 v[42:45], v182 offset:0x80
	ds_read_b128 v[46:49], v182 offset:0x2080
	s_waitcnt lgkmcnt(2)
	v_mfma_f32_32x32x16_bf16 v[16:31], v[54:57], v[238:241], v[16:31]
	v_mfma_f32_32x32x16_bf16 v[0:15], v[58:61], v[238:241], v[0:15]
	ds_read_b128 v[54:57], v183 offset:0x80
	ds_read_b128 v[58:61], v183 offset:0x2080
	s_waitcnt lgkmcnt(2)
	v_mfma_f32_32x32x16_bf16 v[16:31], v[42:45], v[242:245], v[16:31]
	v_mfma_f32_32x32x16_bf16 v[0:15], v[46:49], v[242:245], v[0:15]
	ds_read_b128 v[42:45], v184 offset:0x80
	ds_read_b128 v[46:49], v184 offset:0x2080
	s_waitcnt lgkmcnt(2)
	v_mfma_f32_32x32x16_bf16 v[16:31], v[54:57], v[246:249], v[16:31]
	v_mfma_f32_32x32x16_bf16 v[0:15], v[58:61], v[246:249], v[0:15]
	s_waitcnt lgkmcnt(0)
	v_mfma_f32_32x32x16_bf16 v[16:31], v[42:45], v[166:169], v[16:31]
	v_mfma_f32_32x32x16_bf16 v[0:15], v[46:49], v[166:169], v[0:15]
	s_bitcmp0_b32 s100, 8
	s_cbranch_scc1 .Lstg_a9
	s_waitcnt vmcnt(0)
	s_waitcnt lgkmcnt(0)
	s_barrier
	s_sleep 6

.LBB0_557:
	ds_read_b64_tr_b16 v[144:145], v177 offset:0
	ds_read_b64_tr_b16 v[146:147], v177 offset:0x1000
	ds_read_b64_tr_b16 v[148:149], v177 offset:0x2000
	ds_read_b64_tr_b16 v[150:151], v177 offset:0x3000
	ds_read_b64_tr_b16 v[152:153], v177 offset:0x4000
	ds_read_b64_tr_b16 v[154:155], v177 offset:0x5000
	ds_read_b64_tr_b16 v[156:157], v177 offset:0x6000
	ds_read_b64_tr_b16 v[158:159], v177 offset:0x7000
	s_waitcnt lgkmcnt(6)
	s_nop 0
	v_mfma_f32_32x32x16_bf16 v[112:127], v[144:147], v[128:131], v[112:127]
	ds_read_b64_tr_b16 v[192:193], v177 offset:0x200
	ds_read_b64_tr_b16 v[194:195], v177 offset:0x1200
	s_waitcnt lgkmcnt(6)
	v_mfma_f32_32x32x16_bf16 v[112:127], v[148:151], v[132:135], v[112:127]
	ds_read_b64_tr_b16 v[196:197], v177 offset:0x2200
	ds_read_b64_tr_b16 v[198:199], v177 offset:0x3200
	s_waitcnt lgkmcnt(6)
	v_mfma_f32_32x32x16_bf16 v[112:127], v[152:155], v[136:139], v[112:127]
	ds_read_b64_tr_b16 v[200:201], v177 offset:0x4200
	ds_read_b64_tr_b16 v[202:203], v177 offset:0x5200
	s_waitcnt lgkmcnt(6)
	v_mfma_f32_32x32x16_bf16 v[112:127], v[156:159], v[140:143], v[112:127]
	ds_read_b64_tr_b16 v[204:205], v177 offset:0x6200
	ds_read_b64_tr_b16 v[206:207], v177 offset:0x7200
	s_waitcnt lgkmcnt(6)
	v_mfma_f32_32x32x16_bf16 v[80:95], v[192:195], v[128:131], v[80:95]
	ds_read_b64_tr_b16 v[144:145], v177 offset:0x400
	ds_read_b64_tr_b16 v[146:147], v177 offset:0x1400
	s_waitcnt lgkmcnt(6)
	v_mfma_f32_32x32x16_bf16 v[80:95], v[196:199], v[132:135], v[80:95]
	ds_read_b64_tr_b16 v[148:149], v177 offset:0x2400
	ds_read_b64_tr_b16 v[150:151], v177 offset:0x3400
	s_waitcnt lgkmcnt(6)
	v_mfma_f32_32x32x16_bf16 v[80:95], v[200:203], v[136:139], v[80:95]
	ds_read_b64_tr_b16 v[152:153], v177 offset:0x4400
	ds_read_b64_tr_b16 v[154:155], v177 offset:0x5400
	s_waitcnt lgkmcnt(6)
	v_mfma_f32_32x32x16_bf16 v[80:95], v[204:207], v[140:143], v[80:95]
	ds_read_b64_tr_b16 v[156:157], v177 offset:0x6400
	ds_read_b64_tr_b16 v[158:159], v177 offset:0x7400
	s_waitcnt lgkmcnt(6)
	v_mfma_f32_32x32x16_bf16 v[96:111], v[144:147], v[128:131], v[96:111]
	ds_read_b64_tr_b16 v[192:193], v177 offset:0x600
	ds_read_b64_tr_b16 v[194:195], v177 offset:0x1600
	s_waitcnt lgkmcnt(6)
	v_mfma_f32_32x32x16_bf16 v[96:111], v[148:151], v[132:135], v[96:111]
	ds_read_b64_tr_b16 v[196:197], v177 offset:0x2600
	ds_read_b64_tr_b16 v[198:199], v177 offset:0x3600
	s_waitcnt lgkmcnt(6)
	v_mfma_f32_32x32x16_bf16 v[96:111], v[152:155], v[136:139], v[96:111]
	ds_read_b64_tr_b16 v[200:201], v177 offset:0x4600
	ds_read_b64_tr_b16 v[202:203], v177 offset:0x5600
	s_waitcnt lgkmcnt(6)
	v_mfma_f32_32x32x16_bf16 v[96:111], v[156:159], v[140:143], v[96:111]
	ds_read_b64_tr_b16 v[204:205], v177 offset:0x6600
	ds_read_b64_tr_b16 v[206:207], v177 offset:0x7600
	s_waitcnt lgkmcnt(6)
	v_mfma_f32_32x32x16_bf16 v[64:79], v[192:195], v[128:131], v[64:79]
	ds_read_b64_tr_b16 v[144:145], v177 offset:0x800
	ds_read_b64_tr_b16 v[146:147], v177 offset:0x1800
	s_waitcnt lgkmcnt(6)
	v_mfma_f32_32x32x16_bf16 v[64:79], v[196:199], v[132:135], v[64:79]
	ds_read_b64_tr_b16 v[148:149], v177 offset:0x2800
	ds_read_b64_tr_b16 v[150:151], v177 offset:0x3800
	s_waitcnt lgkmcnt(6)
	v_mfma_f32_32x32x16_bf16 v[64:79], v[200:203], v[136:139], v[64:79]
	ds_read_b64_tr_b16 v[152:153], v177 offset:0x4800
	ds_read_b64_tr_b16 v[154:155], v177 offset:0x5800
	s_waitcnt lgkmcnt(6)
	v_mfma_f32_32x32x16_bf16 v[64:79], v[204:207], v[140:143], v[64:79]
	ds_read_b64_tr_b16 v[156:157], v177 offset:0x6800
	ds_read_b64_tr_b16 v[158:159], v177 offset:0x7800
	s_waitcnt lgkmcnt(6)
	v_mfma_f32_32x32x16_bf16 v[48:63], v[144:147], v[128:131], v[48:63]
	ds_read_b64_tr_b16 v[192:193], v177 offset:0xa00
	ds_read_b64_tr_b16 v[194:195], v177 offset:0x1a00
	s_waitcnt lgkmcnt(6)
	v_mfma_f32_32x32x16_bf16 v[48:63], v[148:151], v[132:135], v[48:63]
	ds_read_b64_tr_b16 v[196:197], v177 offset:0x2a00
	ds_read_b64_tr_b16 v[198:199], v177 offset:0x3a00
	s_waitcnt lgkmcnt(6)
	v_mfma_f32_32x32x16_bf16 v[48:63], v[152:155], v[136:139], v[48:63]
	ds_read_b64_tr_b16 v[200:201], v177 offset:0x4a00
	ds_read_b64_tr_b16 v[202:203], v177 offset:0x5a00
	s_waitcnt lgkmcnt(6)
	v_mfma_f32_32x32x16_bf16 v[48:63], v[156:159], v[140:143], v[48:63]
	ds_read_b64_tr_b16 v[204:205], v177 offset:0x6a00
	ds_read_b64_tr_b16 v[206:207], v177 offset:0x7a00
	s_waitcnt lgkmcnt(6)
	v_mfma_f32_32x32x16_bf16 v[32:47], v[192:195], v[128:131], v[32:47]
	ds_read_b64_tr_b16 v[144:145], v177 offset:0xc00
	ds_read_b64_tr_b16 v[146:147], v177 offset:0x1c00
	s_waitcnt lgkmcnt(6)
	v_mfma_f32_32x32x16_bf16 v[32:47], v[196:199], v[132:135], v[32:47]
	ds_read_b64_tr_b16 v[148:149], v177 offset:0x2c00
	ds_read_b64_tr_b16 v[150:151], v177 offset:0x3c00
	s_waitcnt lgkmcnt(6)
	v_mfma_f32_32x32x16_bf16 v[32:47], v[200:203], v[136:139], v[32:47]
	ds_read_b64_tr_b16 v[152:153], v177 offset:0x4c00
	ds_read_b64_tr_b16 v[154:155], v177 offset:0x5c00
	s_waitcnt lgkmcnt(6)
	v_mfma_f32_32x32x16_bf16 v[32:47], v[204:207], v[140:143], v[32:47]
	ds_read_b64_tr_b16 v[156:157], v177 offset:0x6c00
	ds_read_b64_tr_b16 v[158:159], v177 offset:0x7c00
	s_waitcnt lgkmcnt(6)
	v_mfma_f32_32x32x16_bf16 v[16:31], v[144:147], v[128:131], v[16:31]
	ds_read_b64_tr_b16 v[192:193], v177 offset:0xe00
	ds_read_b64_tr_b16 v[194:195], v177 offset:0x1e00
	s_waitcnt lgkmcnt(6)
	v_mfma_f32_32x32x16_bf16 v[16:31], v[148:151], v[132:135], v[16:31]
	ds_read_b64_tr_b16 v[196:197], v177 offset:0x2e00
	ds_read_b64_tr_b16 v[198:199], v177 offset:0x3e00
	s_waitcnt lgkmcnt(6)
	v_mfma_f32_32x32x16_bf16 v[16:31], v[152:155], v[136:139], v[16:31]
	ds_read_b64_tr_b16 v[200:201], v177 offset:0x4e00
	ds_read_b64_tr_b16 v[202:203], v177 offset:0x5e00
	s_waitcnt lgkmcnt(6)
	v_mfma_f32_32x32x16_bf16 v[16:31], v[156:159], v[140:143], v[16:31]
	ds_read_b64_tr_b16 v[204:205], v177 offset:0x6e00
	ds_read_b64_tr_b16 v[206:207], v177 offset:0x7e00
	s_waitcnt lgkmcnt(6)
	v_mfma_f32_32x32x16_bf16 v[0:15], v[192:195], v[128:131], v[0:15]
	s_waitcnt lgkmcnt(4)
	v_mfma_f32_32x32x16_bf16 v[0:15], v[196:199], v[132:135], v[0:15]
	s_waitcnt lgkmcnt(2)
	v_mfma_f32_32x32x16_bf16 v[0:15], v[200:203], v[136:139], v[0:15]
	s_waitcnt lgkmcnt(0)
	v_mfma_f32_32x32x16_bf16 v[0:15], v[204:207], v[140:143], v[0:15]
	ds_read_b128 v[128:131], v188 offset:0
	ds_read_b128 v[132:135], v188 offset:0x2000
	ds_read_b128 v[192:195], v187 offset:0
	ds_read_b128 v[196:199], v187 offset:0x2000
	s_waitcnt lgkmcnt(2)
	s_nop 0
	v_mfma_f32_32x32x16_bf16 v[144:159], v[128:131], v[218:221], 0
	v_mfma_f32_32x32x16_bf16 v[128:143], v[132:135], v[218:221], 0
	ds_read_b128 v[204:207], v186 offset:0
	ds_read_b128 v[208:211], v186 offset:0x2000
	s_waitcnt lgkmcnt(2)
	v_mfma_f32_32x32x16_bf16 v[144:159], v[192:195], v[222:225], v[144:159]
	v_mfma_f32_32x32x16_bf16 v[128:143], v[196:199], v[222:225], v[128:143]
	ds_read_b128 v[192:195], v185 offset:0
	ds_read_b128 v[196:199], v185 offset:0x2000
	s_waitcnt lgkmcnt(2)
	v_mfma_f32_32x32x16_bf16 v[144:159], v[204:207], v[230:233], v[144:159]
	v_mfma_f32_32x32x16_bf16 v[128:143], v[208:211], v[230:233], v[128:143]
	ds_read_b128 v[204:207], v188 offset:0x80
	ds_read_b128 v[208:211], v188 offset:0x2080
	s_waitcnt lgkmcnt(2)
	v_mfma_f32_32x32x16_bf16 v[144:159], v[192:195], v[234:237], v[144:159]
	v_mfma_f32_32x32x16_bf16 v[128:143], v[196:199], v[234:237], v[128:143]
	ds_read_b128 v[192:195], v187 offset:0x80
	ds_read_b128 v[196:199], v187 offset:0x2080
	s_waitcnt lgkmcnt(2)
	v_mfma_f32_32x32x16_bf16 v[144:159], v[204:207], v[238:241], v[144:159]
	v_mfma_f32_32x32x16_bf16 v[128:143], v[208:211], v[238:241], v[128:143]
	ds_read_b128 v[204:207], v186 offset:0x80
	ds_read_b128 v[208:211], v186 offset:0x2080
	s_waitcnt lgkmcnt(2)
	v_mfma_f32_32x32x16_bf16 v[144:159], v[192:195], v[242:245], v[144:159]
	v_mfma_f32_32x32x16_bf16 v[128:143], v[196:199], v[242:245], v[128:143]
	ds_read_b128 v[192:195], v185 offset:0x80
	ds_read_b128 v[196:199], v185 offset:0x2080
	s_waitcnt lgkmcnt(2)
	v_mfma_f32_32x32x16_bf16 v[144:159], v[204:207], v[246:249], v[144:159]
	v_mfma_f32_32x32x16_bf16 v[128:143], v[208:211], v[246:249], v[128:143]
	s_waitcnt lgkmcnt(0)
	v_mfma_f32_32x32x16_bf16 v[144:159], v[192:195], v[166:169], v[144:159]
	v_mfma_f32_32x32x16_bf16 v[128:143], v[196:199], v[166:169], v[128:143]
	s_bitcmp0_b32 s100, 8
	s_cbranch_scc1 .Lstg_a10
	s_waitcnt vmcnt(0)
	s_waitcnt lgkmcnt(0)
	s_barrier
	s_sleep 6

.LBB0_565:
	ds_read_b64_tr_b16 v[144:145], v177 offset:0x8000
	ds_read_b64_tr_b16 v[146:147], v177 offset:0x9000
	ds_read_b64_tr_b16 v[148:149], v177 offset:0xa000
	ds_read_b64_tr_b16 v[150:151], v177 offset:0xb000
	ds_read_b64_tr_b16 v[152:153], v177 offset:0xc000
	ds_read_b64_tr_b16 v[154:155], v177 offset:0xd000
	ds_read_b64_tr_b16 v[156:157], v177 offset:0xe000
	ds_read_b64_tr_b16 v[158:159], v177 offset:0xf000
	s_waitcnt lgkmcnt(6)
	s_nop 0
	v_mfma_f32_32x32x16_bf16 v[112:127], v[144:147], v[128:131], v[112:127]
	ds_read_b64_tr_b16 v[194:195], v177 offset:0x8200
	ds_read_b64_tr_b16 v[196:197], v177 offset:0x9200
	s_waitcnt lgkmcnt(6)
	v_mfma_f32_32x32x16_bf16 v[112:127], v[148:151], v[132:135], v[112:127]
	ds_read_b64_tr_b16 v[198:199], v177 offset:0xa200
	ds_read_b64_tr_b16 v[200:201], v177 offset:0xb200
	s_waitcnt lgkmcnt(6)
	v_mfma_f32_32x32x16_bf16 v[112:127], v[152:155], v[136:139], v[112:127]
	ds_read_b64_tr_b16 v[202:203], v177 offset:0xc200
	ds_read_b64_tr_b16 v[204:205], v177 offset:0xd200
	s_waitcnt lgkmcnt(6)
	v_mfma_f32_32x32x16_bf16 v[112:127], v[156:159], v[140:143], v[112:127]
	ds_read_b64_tr_b16 v[206:207], v177 offset:0xe200
	ds_read_b64_tr_b16 v[208:209], v177 offset:0xf200
	s_waitcnt lgkmcnt(6)
	v_mfma_f32_32x32x16_bf16 v[80:95], v[194:197], v[128:131], v[80:95]
	ds_read_b64_tr_b16 v[144:145], v177 offset:0x8400
	ds_read_b64_tr_b16 v[146:147], v177 offset:0x9400
	s_waitcnt lgkmcnt(6)
	v_mfma_f32_32x32x16_bf16 v[80:95], v[198:201], v[132:135], v[80:95]
	ds_read_b64_tr_b16 v[148:149], v177 offset:0xa400
	ds_read_b64_tr_b16 v[150:151], v177 offset:0xb400
	s_waitcnt lgkmcnt(6)
	v_mfma_f32_32x32x16_bf16 v[80:95], v[202:205], v[136:139], v[80:95]
	ds_read_b64_tr_b16 v[152:153], v177 offset:0xc400
	ds_read_b64_tr_b16 v[154:155], v177 offset:0xd400
	s_waitcnt lgkmcnt(6)
	v_mfma_f32_32x32x16_bf16 v[80:95], v[206:209], v[140:143], v[80:95]
	ds_read_b64_tr_b16 v[156:157], v177 offset:0xe400
	ds_read_b64_tr_b16 v[158:159], v177 offset:0xf400
	s_waitcnt lgkmcnt(6)
	v_mfma_f32_32x32x16_bf16 v[96:111], v[144:147], v[128:131], v[96:111]
	ds_read_b64_tr_b16 v[194:195], v177 offset:0x8600
	ds_read_b64_tr_b16 v[196:197], v177 offset:0x9600
	s_waitcnt lgkmcnt(6)
	v_mfma_f32_32x32x16_bf16 v[96:111], v[148:151], v[132:135], v[96:111]
	ds_read_b64_tr_b16 v[198:199], v177 offset:0xa600
	ds_read_b64_tr_b16 v[200:201], v177 offset:0xb600
	s_waitcnt lgkmcnt(6)
	v_mfma_f32_32x32x16_bf16 v[96:111], v[152:155], v[136:139], v[96:111]
	ds_read_b64_tr_b16 v[202:203], v177 offset:0xc600
	ds_read_b64_tr_b16 v[204:205], v177 offset:0xd600
	s_waitcnt lgkmcnt(6)
	v_mfma_f32_32x32x16_bf16 v[96:111], v[156:159], v[140:143], v[96:111]
	ds_read_b64_tr_b16 v[206:207], v177 offset:0xe600
	ds_read_b64_tr_b16 v[208:209], v177 offset:0xf600
	s_waitcnt lgkmcnt(6)
	v_mfma_f32_32x32x16_bf16 v[64:79], v[194:197], v[128:131], v[64:79]
	ds_read_b64_tr_b16 v[144:145], v177 offset:0x8800
	ds_read_b64_tr_b16 v[146:147], v177 offset:0x9800
	s_waitcnt lgkmcnt(6)
	v_mfma_f32_32x32x16_bf16 v[64:79], v[198:201], v[132:135], v[64:79]
	ds_read_b64_tr_b16 v[148:149], v177 offset:0xa800
	ds_read_b64_tr_b16 v[150:151], v177 offset:0xb800
	s_waitcnt lgkmcnt(6)
	v_mfma_f32_32x32x16_bf16 v[64:79], v[202:205], v[136:139], v[64:79]
	ds_read_b64_tr_b16 v[152:153], v177 offset:0xc800
	ds_read_b64_tr_b16 v[154:155], v177 offset:0xd800
	s_waitcnt lgkmcnt(6)
	v_mfma_f32_32x32x16_bf16 v[64:79], v[206:209], v[140:143], v[64:79]
	ds_read_b64_tr_b16 v[156:157], v177 offset:0xe800
	ds_read_b64_tr_b16 v[158:159], v177 offset:0xf800
	s_waitcnt lgkmcnt(6)
	v_mfma_f32_32x32x16_bf16 v[48:63], v[144:147], v[128:131], v[48:63]
	ds_read_b64_tr_b16 v[194:195], v177 offset:0x8a00
	ds_read_b64_tr_b16 v[196:197], v177 offset:0x9a00
	s_waitcnt lgkmcnt(6)
	v_mfma_f32_32x32x16_bf16 v[48:63], v[148:151], v[132:135], v[48:63]
	ds_read_b64_tr_b16 v[198:199], v177 offset:0xaa00
	ds_read_b64_tr_b16 v[200:201], v177 offset:0xba00
	s_waitcnt lgkmcnt(6)
	v_mfma_f32_32x32x16_bf16 v[48:63], v[152:155], v[136:139], v[48:63]
	ds_read_b64_tr_b16 v[202:203], v177 offset:0xca00
	ds_read_b64_tr_b16 v[204:205], v177 offset:0xda00
	s_waitcnt lgkmcnt(6)
	v_mfma_f32_32x32x16_bf16 v[48:63], v[156:159], v[140:143], v[48:63]
	ds_read_b64_tr_b16 v[206:207], v177 offset:0xea00
	ds_read_b64_tr_b16 v[208:209], v177 offset:0xfa00
	s_waitcnt lgkmcnt(6)
	v_mfma_f32_32x32x16_bf16 v[32:47], v[194:197], v[128:131], v[32:47]
	ds_read_b64_tr_b16 v[144:145], v177 offset:0x8c00
	ds_read_b64_tr_b16 v[146:147], v177 offset:0x9c00
	s_waitcnt lgkmcnt(6)
	v_mfma_f32_32x32x16_bf16 v[32:47], v[198:201], v[132:135], v[32:47]
	ds_read_b64_tr_b16 v[148:149], v177 offset:0xac00
	ds_read_b64_tr_b16 v[150:151], v177 offset:0xbc00
	s_waitcnt lgkmcnt(6)
	v_mfma_f32_32x32x16_bf16 v[32:47], v[202:205], v[136:139], v[32:47]
	ds_read_b64_tr_b16 v[152:153], v177 offset:0xcc00
	ds_read_b64_tr_b16 v[154:155], v177 offset:0xdc00
	s_waitcnt lgkmcnt(6)
	v_mfma_f32_32x32x16_bf16 v[32:47], v[206:209], v[140:143], v[32:47]
	ds_read_b64_tr_b16 v[156:157], v177 offset:0xec00
	ds_read_b64_tr_b16 v[158:159], v177 offset:0xfc00
	s_waitcnt lgkmcnt(6)
	v_mfma_f32_32x32x16_bf16 v[16:31], v[144:147], v[128:131], v[16:31]
	ds_read_b64_tr_b16 v[194:195], v177 offset:0x8e00
	ds_read_b64_tr_b16 v[196:197], v177 offset:0x9e00
	s_waitcnt lgkmcnt(6)
	v_mfma_f32_32x32x16_bf16 v[16:31], v[148:151], v[132:135], v[16:31]
	ds_read_b64_tr_b16 v[198:199], v177 offset:0xae00
	ds_read_b64_tr_b16 v[200:201], v177 offset:0xbe00
	s_waitcnt lgkmcnt(6)
	v_mfma_f32_32x32x16_bf16 v[16:31], v[152:155], v[136:139], v[16:31]
	ds_read_b64_tr_b16 v[202:203], v177 offset:0xce00
	ds_read_b64_tr_b16 v[204:205], v177 offset:0xde00
	s_waitcnt lgkmcnt(6)
	v_mfma_f32_32x32x16_bf16 v[16:31], v[156:159], v[140:143], v[16:31]
	ds_read_b64_tr_b16 v[206:207], v177 offset:0xee00
	ds_read_b64_tr_b16 v[208:209], v177 offset:0xfe00
	s_waitcnt lgkmcnt(6)
	v_mfma_f32_32x32x16_bf16 v[0:15], v[194:197], v[128:131], v[0:15]
	s_waitcnt lgkmcnt(4)
	v_mfma_f32_32x32x16_bf16 v[0:15], v[198:201], v[132:135], v[0:15]
	s_waitcnt lgkmcnt(2)
	v_mfma_f32_32x32x16_bf16 v[0:15], v[202:205], v[136:139], v[0:15]
	s_waitcnt lgkmcnt(0)
	v_mfma_f32_32x32x16_bf16 v[0:15], v[206:209], v[140:143], v[0:15]
	ds_read_b128 v[128:131], v181 offset:0
	ds_read_b128 v[132:135], v181 offset:0x2000
	ds_read_b128 v[194:197], v182 offset:0
	ds_read_b128 v[198:201], v182 offset:0x2000
	s_waitcnt lgkmcnt(2)
	s_nop 0
	v_mfma_f32_32x32x16_bf16 v[144:159], v[128:131], v[218:221], 0
	v_mfma_f32_32x32x16_bf16 v[128:143], v[132:135], v[218:221], 0
	ds_read_b128 v[206:209], v183 offset:0
	ds_read_b128 v[210:213], v183 offset:0x2000
	s_waitcnt lgkmcnt(2)
	v_mfma_f32_32x32x16_bf16 v[144:159], v[194:197], v[222:225], v[144:159]
	v_mfma_f32_32x32x16_bf16 v[128:143], v[198:201], v[222:225], v[128:143]
	ds_read_b128 v[194:197], v184 offset:0
	ds_read_b128 v[198:201], v184 offset:0x2000
	s_waitcnt lgkmcnt(2)
	v_mfma_f32_32x32x16_bf16 v[144:159], v[206:209], v[230:233], v[144:159]
	v_mfma_f32_32x32x16_bf16 v[128:143], v[210:213], v[230:233], v[128:143]
	ds_read_b128 v[206:209], v181 offset:0x80
	ds_read_b128 v[210:213], v181 offset:0x2080
	s_waitcnt lgkmcnt(2)
	v_mfma_f32_32x32x16_bf16 v[144:159], v[194:197], v[234:237], v[144:159]
	v_mfma_f32_32x32x16_bf16 v[128:143], v[198:201], v[234:237], v[128:143]
	ds_read_b128 v[194:197], v182 offset:0x80
	ds_read_b128 v[198:201], v182 offset:0x2080
	s_waitcnt lgkmcnt(2)
	v_mfma_f32_32x32x16_bf16 v[144:159], v[206:209], v[238:241], v[144:159]
	v_mfma_f32_32x32x16_bf16 v[128:143], v[210:213], v[238:241], v[128:143]
	ds_read_b128 v[206:209], v183 offset:0x80
	ds_read_b128 v[210:213], v183 offset:0x2080
	s_waitcnt lgkmcnt(2)
	v_mfma_f32_32x32x16_bf16 v[144:159], v[194:197], v[242:245], v[144:159]
	v_mfma_f32_32x32x16_bf16 v[128:143], v[198:201], v[242:245], v[128:143]
	ds_read_b128 v[194:197], v184 offset:0x80
	ds_read_b128 v[198:201], v184 offset:0x2080
	s_waitcnt lgkmcnt(2)
	v_mfma_f32_32x32x16_bf16 v[144:159], v[206:209], v[246:249], v[144:159]
	v_mfma_f32_32x32x16_bf16 v[128:143], v[210:213], v[246:249], v[128:143]
	s_waitcnt lgkmcnt(0)
	v_mfma_f32_32x32x16_bf16 v[144:159], v[194:197], v[166:169], v[144:159]
	v_mfma_f32_32x32x16_bf16 v[128:143], v[198:201], v[166:169], v[128:143]
	s_bitcmp0_b32 s100, 8
	s_cbranch_scc1 .Lstg_a11
	s_waitcnt vmcnt(0)
	s_waitcnt lgkmcnt(0)
	s_barrier
	s_sleep 6

.LBB0_580:
	ds_read_b64_tr_b16 v[144:145], v177 offset:0
	ds_read_b64_tr_b16 v[146:147], v177 offset:0x1000
	ds_read_b64_tr_b16 v[148:149], v177 offset:0x2000
	ds_read_b64_tr_b16 v[150:151], v177 offset:0x3000
	ds_read_b64_tr_b16 v[152:153], v177 offset:0x4000
	ds_read_b64_tr_b16 v[154:155], v177 offset:0x5000
	ds_read_b64_tr_b16 v[156:157], v177 offset:0x6000
	ds_read_b64_tr_b16 v[158:159], v177 offset:0x7000
	s_waitcnt lgkmcnt(6)
	s_nop 0
	v_mfma_f32_32x32x16_bf16 v[112:127], v[144:147], v[128:131], v[112:127]
	ds_read_b64_tr_b16 v[192:193], v177 offset:0x200
	ds_read_b64_tr_b16 v[194:195], v177 offset:0x1200
	s_waitcnt lgkmcnt(6)
	v_mfma_f32_32x32x16_bf16 v[112:127], v[148:151], v[132:135], v[112:127]
	ds_read_b64_tr_b16 v[196:197], v177 offset:0x2200
	ds_read_b64_tr_b16 v[198:199], v177 offset:0x3200
	s_waitcnt lgkmcnt(6)
	v_mfma_f32_32x32x16_bf16 v[112:127], v[152:155], v[136:139], v[112:127]
	ds_read_b64_tr_b16 v[200:201], v177 offset:0x4200
	ds_read_b64_tr_b16 v[202:203], v177 offset:0x5200
	s_waitcnt lgkmcnt(6)
	v_mfma_f32_32x32x16_bf16 v[112:127], v[156:159], v[140:143], v[112:127]
	ds_read_b64_tr_b16 v[204:205], v177 offset:0x6200
	ds_read_b64_tr_b16 v[206:207], v177 offset:0x7200
	s_waitcnt lgkmcnt(6)
	v_mfma_f32_32x32x16_bf16 v[80:95], v[192:195], v[128:131], v[80:95]
	ds_read_b64_tr_b16 v[144:145], v177 offset:0x400
	ds_read_b64_tr_b16 v[146:147], v177 offset:0x1400
	s_waitcnt lgkmcnt(6)
	v_mfma_f32_32x32x16_bf16 v[80:95], v[196:199], v[132:135], v[80:95]
	ds_read_b64_tr_b16 v[148:149], v177 offset:0x2400
	ds_read_b64_tr_b16 v[150:151], v177 offset:0x3400
	s_waitcnt lgkmcnt(6)
	v_mfma_f32_32x32x16_bf16 v[80:95], v[200:203], v[136:139], v[80:95]
	ds_read_b64_tr_b16 v[152:153], v177 offset:0x4400
	ds_read_b64_tr_b16 v[154:155], v177 offset:0x5400
	s_waitcnt lgkmcnt(6)
	v_mfma_f32_32x32x16_bf16 v[80:95], v[204:207], v[140:143], v[80:95]
	ds_read_b64_tr_b16 v[156:157], v177 offset:0x6400
	ds_read_b64_tr_b16 v[158:159], v177 offset:0x7400
	s_waitcnt lgkmcnt(6)
	v_mfma_f32_32x32x16_bf16 v[96:111], v[144:147], v[128:131], v[96:111]
	ds_read_b64_tr_b16 v[192:193], v177 offset:0x600
	ds_read_b64_tr_b16 v[194:195], v177 offset:0x1600
	s_waitcnt lgkmcnt(6)
	v_mfma_f32_32x32x16_bf16 v[96:111], v[148:151], v[132:135], v[96:111]
	ds_read_b64_tr_b16 v[196:197], v177 offset:0x2600
	ds_read_b64_tr_b16 v[198:199], v177 offset:0x3600
	s_waitcnt lgkmcnt(6)
	v_mfma_f32_32x32x16_bf16 v[96:111], v[152:155], v[136:139], v[96:111]
	ds_read_b64_tr_b16 v[200:201], v177 offset:0x4600
	ds_read_b64_tr_b16 v[202:203], v177 offset:0x5600
	s_waitcnt lgkmcnt(6)
	v_mfma_f32_32x32x16_bf16 v[96:111], v[156:159], v[140:143], v[96:111]
	ds_read_b64_tr_b16 v[204:205], v177 offset:0x6600
	ds_read_b64_tr_b16 v[206:207], v177 offset:0x7600
	s_waitcnt lgkmcnt(6)
	v_mfma_f32_32x32x16_bf16 v[64:79], v[192:195], v[128:131], v[64:79]
	ds_read_b64_tr_b16 v[144:145], v177 offset:0x800
	ds_read_b64_tr_b16 v[146:147], v177 offset:0x1800
	s_waitcnt lgkmcnt(6)
	v_mfma_f32_32x32x16_bf16 v[64:79], v[196:199], v[132:135], v[64:79]
	ds_read_b64_tr_b16 v[148:149], v177 offset:0x2800
	ds_read_b64_tr_b16 v[150:151], v177 offset:0x3800
	s_waitcnt lgkmcnt(6)
	v_mfma_f32_32x32x16_bf16 v[64:79], v[200:203], v[136:139], v[64:79]
	ds_read_b64_tr_b16 v[152:153], v177 offset:0x4800
	ds_read_b64_tr_b16 v[154:155], v177 offset:0x5800
	s_waitcnt lgkmcnt(6)
	v_mfma_f32_32x32x16_bf16 v[64:79], v[204:207], v[140:143], v[64:79]
	ds_read_b64_tr_b16 v[156:157], v177 offset:0x6800
	ds_read_b64_tr_b16 v[158:159], v177 offset:0x7800
	s_waitcnt lgkmcnt(6)
	v_mfma_f32_32x32x16_bf16 v[48:63], v[144:147], v[128:131], v[48:63]
	ds_read_b64_tr_b16 v[192:193], v177 offset:0xa00
	ds_read_b64_tr_b16 v[194:195], v177 offset:0x1a00
	s_waitcnt lgkmcnt(6)
	v_mfma_f32_32x32x16_bf16 v[48:63], v[148:151], v[132:135], v[48:63]
	ds_read_b64_tr_b16 v[196:197], v177 offset:0x2a00
	ds_read_b64_tr_b16 v[198:199], v177 offset:0x3a00
	s_waitcnt lgkmcnt(6)
	v_mfma_f32_32x32x16_bf16 v[48:63], v[152:155], v[136:139], v[48:63]
	ds_read_b64_tr_b16 v[200:201], v177 offset:0x4a00
	ds_read_b64_tr_b16 v[202:203], v177 offset:0x5a00
	s_waitcnt lgkmcnt(6)
	v_mfma_f32_32x32x16_bf16 v[48:63], v[156:159], v[140:143], v[48:63]
	ds_read_b64_tr_b16 v[204:205], v177 offset:0x6a00
	ds_read_b64_tr_b16 v[206:207], v177 offset:0x7a00
	s_waitcnt lgkmcnt(6)
	v_mfma_f32_32x32x16_bf16 v[32:47], v[192:195], v[128:131], v[32:47]
	ds_read_b64_tr_b16 v[144:145], v177 offset:0xc00
	ds_read_b64_tr_b16 v[146:147], v177 offset:0x1c00
	s_waitcnt lgkmcnt(6)
	v_mfma_f32_32x32x16_bf16 v[32:47], v[196:199], v[132:135], v[32:47]
	ds_read_b64_tr_b16 v[148:149], v177 offset:0x2c00
	ds_read_b64_tr_b16 v[150:151], v177 offset:0x3c00
	s_waitcnt lgkmcnt(6)
	v_mfma_f32_32x32x16_bf16 v[32:47], v[200:203], v[136:139], v[32:47]
	ds_read_b64_tr_b16 v[152:153], v177 offset:0x4c00
	ds_read_b64_tr_b16 v[154:155], v177 offset:0x5c00
	s_waitcnt lgkmcnt(6)
	v_mfma_f32_32x32x16_bf16 v[32:47], v[204:207], v[140:143], v[32:47]
	ds_read_b64_tr_b16 v[156:157], v177 offset:0x6c00
	ds_read_b64_tr_b16 v[158:159], v177 offset:0x7c00
	s_waitcnt lgkmcnt(6)
	v_mfma_f32_32x32x16_bf16 v[16:31], v[144:147], v[128:131], v[16:31]
	ds_read_b64_tr_b16 v[192:193], v177 offset:0xe00
	ds_read_b64_tr_b16 v[194:195], v177 offset:0x1e00
	s_waitcnt lgkmcnt(6)
	v_mfma_f32_32x32x16_bf16 v[16:31], v[148:151], v[132:135], v[16:31]
	ds_read_b64_tr_b16 v[196:197], v177 offset:0x2e00
	ds_read_b64_tr_b16 v[198:199], v177 offset:0x3e00
	s_waitcnt lgkmcnt(6)
	v_mfma_f32_32x32x16_bf16 v[16:31], v[152:155], v[136:139], v[16:31]
	ds_read_b64_tr_b16 v[200:201], v177 offset:0x4e00
	ds_read_b64_tr_b16 v[202:203], v177 offset:0x5e00
	s_waitcnt lgkmcnt(6)
	v_mfma_f32_32x32x16_bf16 v[16:31], v[156:159], v[140:143], v[16:31]
	ds_read_b64_tr_b16 v[204:205], v177 offset:0x6e00
	ds_read_b64_tr_b16 v[206:207], v177 offset:0x7e00
	s_waitcnt lgkmcnt(6)
	v_mfma_f32_32x32x16_bf16 v[0:15], v[192:195], v[128:131], v[0:15]
	s_waitcnt lgkmcnt(4)
	v_mfma_f32_32x32x16_bf16 v[0:15], v[196:199], v[132:135], v[0:15]
	s_waitcnt lgkmcnt(2)
	v_mfma_f32_32x32x16_bf16 v[0:15], v[200:203], v[136:139], v[0:15]
	s_waitcnt lgkmcnt(0)
	v_mfma_f32_32x32x16_bf16 v[0:15], v[204:207], v[140:143], v[0:15]
	ds_read_b128 v[128:131], v188 offset:0
	ds_read_b128 v[132:135], v188 offset:0x2000
	ds_read_b128 v[192:195], v187 offset:0
	ds_read_b128 v[196:199], v187 offset:0x2000
	s_waitcnt lgkmcnt(2)
	s_nop 0
	v_mfma_f32_32x32x16_bf16 v[144:159], v[128:131], v[218:221], 0
	v_mfma_f32_32x32x16_bf16 v[128:143], v[132:135], v[218:221], 0
	ds_read_b128 v[204:207], v186 offset:0
	ds_read_b128 v[208:211], v186 offset:0x2000
	s_waitcnt lgkmcnt(2)
	v_mfma_f32_32x32x16_bf16 v[144:159], v[192:195], v[222:225], v[144:159]
	v_mfma_f32_32x32x16_bf16 v[128:143], v[196:199], v[222:225], v[128:143]
	ds_read_b128 v[192:195], v185 offset:0
	ds_read_b128 v[196:199], v185 offset:0x2000
	s_waitcnt lgkmcnt(2)
	v_mfma_f32_32x32x16_bf16 v[144:159], v[204:207], v[230:233], v[144:159]
	v_mfma_f32_32x32x16_bf16 v[128:143], v[208:211], v[230:233], v[128:143]
	ds_read_b128 v[204:207], v188 offset:0x80
	ds_read_b128 v[208:211], v188 offset:0x2080
	s_waitcnt lgkmcnt(2)
	v_mfma_f32_32x32x16_bf16 v[144:159], v[192:195], v[234:237], v[144:159]
	v_mfma_f32_32x32x16_bf16 v[128:143], v[196:199], v[234:237], v[128:143]
	ds_read_b128 v[192:195], v187 offset:0x80
	ds_read_b128 v[196:199], v187 offset:0x2080
	s_waitcnt lgkmcnt(2)
	v_mfma_f32_32x32x16_bf16 v[144:159], v[204:207], v[238:241], v[144:159]
	v_mfma_f32_32x32x16_bf16 v[128:143], v[208:211], v[238:241], v[128:143]
	ds_read_b128 v[204:207], v186 offset:0x80
	ds_read_b128 v[208:211], v186 offset:0x2080
	s_waitcnt lgkmcnt(2)
	v_mfma_f32_32x32x16_bf16 v[144:159], v[192:195], v[242:245], v[144:159]
	v_mfma_f32_32x32x16_bf16 v[128:143], v[196:199], v[242:245], v[128:143]
	ds_read_b128 v[180:183], v185 offset:0x80
	ds_read_b128 v[192:195], v185 offset:0x2080
	s_waitcnt lgkmcnt(2)
	v_mfma_f32_32x32x16_bf16 v[144:159], v[204:207], v[246:249], v[144:159]
	v_mfma_f32_32x32x16_bf16 v[128:143], v[208:211], v[246:249], v[128:143]
	s_waitcnt lgkmcnt(0)
	v_mfma_f32_32x32x16_bf16 v[144:159], v[180:183], v[166:169], v[144:159]
	v_mfma_f32_32x32x16_bf16 v[128:143], v[192:195], v[166:169], v[128:143]
	s_bitcmp0_b32 s100, 8
	s_cbranch_scc1 .Lstg_a12
	s_waitcnt vmcnt(0)
	s_waitcnt lgkmcnt(0)
	s_barrier
	s_sleep 6

.LBB0_586:
	s_or_b64 exec, exec, s[4:5]
	v_mov_b32_e32 v38, v165
	v_readlane_b32 s5, v255, 51
	v_readfirstlane_b32 s2, v38
	s_ashr_i32 s79, s2, 6
	v_bfe_u32 v0, v38, 5, 1
	v_and_b32_e32 v176, 31, v38
	s_lshl_b32 s92, s79, 5
	v_lshlrev_b32_e32 v32, 2, v0
	s_add_i32 s74, s92, s74
	v_sub_u32_e32 v1, v176, v32
	v_lshlrev_b32_e32 v175, 4, v0
	s_lshl_b32 s2, s79, 3
	v_bfe_u32 v0, v38, 4, 2
	v_add_u32_e32 v179, s74, v1
	v_or_b32_e32 v1, s2, v0
	v_and_b32_e32 v2, 15, v38
	v_and_b32_e32 v39, 63, v38
	v_bitop3_b32 v3, v0, v38, 15 bitop3:0x78
	v_mul_lo_u32 v1, v1, s14
	v_bitop3_b32 v0, v0, v2, 4 bitop3:0x36
	s_mul_i32 s4, s79, 0x1c00
	s_waitcnt vmcnt(16)
	v_lshlrev_b32_e32 v40, 4, v39
	v_lshl_or_b32 v0, v0, 4, v1
	s_lshl_b32 s78, s79, 11
	v_readlane_b32 s7, v255, 53
	s_lshl_b32 s3, s79, 12
	s_add_i32 s4, s5, s4
	v_lshl_or_b32 v160, v3, 4, v1
	v_add_u32_e32 v170, 0x1a000, v0
	s_add_i32 s78, s78, s7
	s_add_i32 s3, s3, s33
	v_add_u32_e32 v180, s4, v40
	s_waitcnt vmcnt(16) lgkmcnt(0)
	v_mov_b64_e32 v[218:219], v[128:129]
	v_mov_b64_e32 v[220:221], v[130:131]
	v_mov_b64_e32 v[222:223], v[132:133]
	v_mov_b64_e32 v[224:225], v[134:135]
	v_mov_b64_e32 v[230:231], v[136:137]
	v_mov_b64_e32 v[232:233], v[138:139]
	v_mov_b64_e32 v[234:235], v[140:141]
	v_mov_b64_e32 v[236:237], v[142:143]
	v_mov_b64_e32 v[238:239], v[144:145]
	v_mov_b64_e32 v[240:241], v[146:147]
	v_mov_b64_e32 v[242:243], v[148:149]
	v_mov_b64_e32 v[244:245], v[150:151]
	v_mov_b64_e32 v[246:247], v[152:153]
	v_mov_b64_e32 v[248:249], v[154:155]
	s_add_u32 s4, s66, 0x1a2900
	s_addc_u32 s5, s67, 0
	v_lshl_add_u64 v[0:1], s[4:5], 0, v[160:161]
	s_add_i32 s82, s78, 0x4000
	s_mov_b32 s6, m0
	s_mov_b32 m0, s82
	s_nop 0
	global_load_lds_dwordx4 v[0:1], off
	s_mov_b32 m0, s6
	v_mov_b32_e32 v171, v161
	v_lshl_add_u64 v[0:1], s[4:5], 0, v[170:171]
	s_add_i32 s84, s78, 0x4400
	s_mov_b32 s4, m0
	s_mov_b32 m0, s84
	s_nop 0
	global_load_lds_dwordx4 v[0:1], off
	s_mov_b32 m0, s4
	s_waitcnt lgkmcnt(0)
	s_barrier
	v_lshlrev_b32_e32 v0, 4, v38
	s_movk_i32 s4, 0x70
	v_lshlrev_b32_e32 v33, 8, v176
	v_and_b32_e32 v1, 0x70, v0
	v_bitop3_b32 v34, v175, v0, s4 bitop3:0x78
	s_movk_i32 s4, 0x60
	v_add_u32_e32 v2, s7, v33
	v_bitop3_b32 v35, v175, v1, 32 bitop3:0x36
	v_bitop3_b32 v36, v175, v1, 64 bitop3:0x36
	v_bitop3_b32 v37, v175, v1, s4 bitop3:0x36
	v_add_u32_e32 v181, v34, v2
	v_add_u32_e32 v182, v35, v2
	v_add_u32_e32 v183, v36, v2
	v_add_u32_e32 v184, v37, v2
	ds_read_b128 v[0:3], v181 offset:0
	ds_read_b128 v[4:7], v181 offset:0x2000
	ds_read_b128 v[42:45], v182 offset:0
	ds_read_b128 v[46:49], v182 offset:0x2000
	s_waitcnt lgkmcnt(2)
	s_nop 0
	v_mfma_f32_32x32x16_bf16 v[16:31], v[0:3], v[218:221], 0
	v_mfma_f32_32x32x16_bf16 v[0:15], v[4:7], v[218:221], 0
	ds_read_b128 v[54:57], v183 offset:0
	ds_read_b128 v[58:61], v183 offset:0x2000
	s_waitcnt lgkmcnt(2)
	v_mfma_f32_32x32x16_bf16 v[16:31], v[42:45], v[222:225], v[16:31]
	v_mfma_f32_32x32x16_bf16 v[0:15], v[46:49], v[222:225], v[0:15]
	ds_read_b128 v[42:45], v184 offset:0
	ds_read_b128 v[46:49], v184 offset:0x2000
	s_waitcnt lgkmcnt(2)
	v_mfma_f32_32x32x16_bf16 v[16:31], v[54:57], v[230:233], v[16:31]
	v_mfma_f32_32x32x16_bf16 v[0:15], v[58:61], v[230:233], v[0:15]
	ds_read_b128 v[54:57], v181 offset:0x80
	ds_read_b128 v[58:61], v181 offset:0x2080
	s_waitcnt lgkmcnt(2)
	v_mfma_f32_32x32x16_bf16 v[16:31], v[42:45], v[234:237], v[16:31]
	v_mfma_f32_32x32x16_bf16 v[0:15], v[46:49], v[234:237], v[0:15]
	ds_read_b128 v[42:45], v182 offset:0x80
	ds_read_b128 v[46:49], v182 offset:0x2080
	s_waitcnt lgkmcnt(2)
	v_mfma_f32_32x32x16_bf16 v[16:31], v[54:57], v[238:241], v[16:31]
	v_mfma_f32_32x32x16_bf16 v[0:15], v[58:61], v[238:241], v[0:15]
	ds_read_b128 v[54:57], v183 offset:0x80
	ds_read_b128 v[58:61], v183 offset:0x2080
	s_waitcnt lgkmcnt(2)
	v_mfma_f32_32x32x16_bf16 v[16:31], v[42:45], v[242:245], v[16:31]
	v_mfma_f32_32x32x16_bf16 v[0:15], v[46:49], v[242:245], v[0:15]
	ds_read_b128 v[42:45], v184 offset:0x80
	ds_read_b128 v[46:49], v184 offset:0x2080
	s_waitcnt lgkmcnt(2)
	v_mfma_f32_32x32x16_bf16 v[16:31], v[54:57], v[246:249], v[16:31]
	v_mfma_f32_32x32x16_bf16 v[0:15], v[58:61], v[246:249], v[0:15]
	s_waitcnt lgkmcnt(0)
	v_mfma_f32_32x32x16_bf16 v[16:31], v[42:45], v[166:169], v[16:31]
	v_mfma_f32_32x32x16_bf16 v[0:15], v[46:49], v[166:169], v[0:15]
	s_bitcmp0_b32 s100, 8
	s_cbranch_scc1 .Lstg_a17
	s_waitcnt vmcnt(0)
	s_waitcnt lgkmcnt(0)
	s_barrier
	s_sleep 6

.LBB0_589:
	ds_read_b64_tr_b16 v[144:145], v177 offset:0
	ds_read_b64_tr_b16 v[146:147], v177 offset:0x1000
	ds_read_b64_tr_b16 v[148:149], v177 offset:0x2000
	ds_read_b64_tr_b16 v[150:151], v177 offset:0x3000
	ds_read_b64_tr_b16 v[152:153], v177 offset:0x4000
	ds_read_b64_tr_b16 v[154:155], v177 offset:0x5000
	ds_read_b64_tr_b16 v[156:157], v177 offset:0x6000
	ds_read_b64_tr_b16 v[158:159], v177 offset:0x7000
	s_waitcnt lgkmcnt(6)
	s_nop 0
	v_mfma_f32_32x32x16_bf16 v[112:127], v[144:147], v[128:131], v[112:127]
	ds_read_b64_tr_b16 v[192:193], v177 offset:0x200
	ds_read_b64_tr_b16 v[194:195], v177 offset:0x1200
	s_waitcnt lgkmcnt(6)
	v_mfma_f32_32x32x16_bf16 v[112:127], v[148:151], v[132:135], v[112:127]
	ds_read_b64_tr_b16 v[196:197], v177 offset:0x2200
	ds_read_b64_tr_b16 v[198:199], v177 offset:0x3200
	s_waitcnt lgkmcnt(6)
	v_mfma_f32_32x32x16_bf16 v[112:127], v[152:155], v[136:139], v[112:127]
	ds_read_b64_tr_b16 v[200:201], v177 offset:0x4200
	ds_read_b64_tr_b16 v[202:203], v177 offset:0x5200
	s_waitcnt lgkmcnt(6)
	v_mfma_f32_32x32x16_bf16 v[112:127], v[156:159], v[140:143], v[112:127]
	ds_read_b64_tr_b16 v[204:205], v177 offset:0x6200
	ds_read_b64_tr_b16 v[206:207], v177 offset:0x7200
	s_waitcnt lgkmcnt(6)
	v_mfma_f32_32x32x16_bf16 v[96:111], v[192:195], v[128:131], v[96:111]
	ds_read_b64_tr_b16 v[144:145], v177 offset:0x400
	ds_read_b64_tr_b16 v[146:147], v177 offset:0x1400
	s_waitcnt lgkmcnt(6)
	v_mfma_f32_32x32x16_bf16 v[96:111], v[196:199], v[132:135], v[96:111]
	ds_read_b64_tr_b16 v[148:149], v177 offset:0x2400
	ds_read_b64_tr_b16 v[150:151], v177 offset:0x3400
	s_waitcnt lgkmcnt(6)
	v_mfma_f32_32x32x16_bf16 v[96:111], v[200:203], v[136:139], v[96:111]
	ds_read_b64_tr_b16 v[152:153], v177 offset:0x4400
	ds_read_b64_tr_b16 v[154:155], v177 offset:0x5400
	s_waitcnt lgkmcnt(6)
	v_mfma_f32_32x32x16_bf16 v[96:111], v[204:207], v[140:143], v[96:111]
	ds_read_b64_tr_b16 v[156:157], v177 offset:0x6400
	ds_read_b64_tr_b16 v[158:159], v177 offset:0x7400
	s_waitcnt lgkmcnt(6)
	v_mfma_f32_32x32x16_bf16 v[80:95], v[144:147], v[128:131], v[80:95]
	ds_read_b64_tr_b16 v[192:193], v177 offset:0x600
	ds_read_b64_tr_b16 v[194:195], v177 offset:0x1600
	s_waitcnt lgkmcnt(6)
	v_mfma_f32_32x32x16_bf16 v[80:95], v[148:151], v[132:135], v[80:95]
	ds_read_b64_tr_b16 v[196:197], v177 offset:0x2600
	ds_read_b64_tr_b16 v[198:199], v177 offset:0x3600
	s_waitcnt lgkmcnt(6)
	v_mfma_f32_32x32x16_bf16 v[80:95], v[152:155], v[136:139], v[80:95]
	ds_read_b64_tr_b16 v[200:201], v177 offset:0x4600
	ds_read_b64_tr_b16 v[202:203], v177 offset:0x5600
	s_waitcnt lgkmcnt(6)
	v_mfma_f32_32x32x16_bf16 v[80:95], v[156:159], v[140:143], v[80:95]
	ds_read_b64_tr_b16 v[204:205], v177 offset:0x6600
	ds_read_b64_tr_b16 v[206:207], v177 offset:0x7600
	s_waitcnt lgkmcnt(6)
	v_mfma_f32_32x32x16_bf16 v[64:79], v[192:195], v[128:131], v[64:79]
	ds_read_b64_tr_b16 v[144:145], v177 offset:0x800
	ds_read_b64_tr_b16 v[146:147], v177 offset:0x1800
	s_waitcnt lgkmcnt(6)
	v_mfma_f32_32x32x16_bf16 v[64:79], v[196:199], v[132:135], v[64:79]
	ds_read_b64_tr_b16 v[148:149], v177 offset:0x2800
	ds_read_b64_tr_b16 v[150:151], v177 offset:0x3800
	s_waitcnt lgkmcnt(6)
	v_mfma_f32_32x32x16_bf16 v[64:79], v[200:203], v[136:139], v[64:79]
	ds_read_b64_tr_b16 v[152:153], v177 offset:0x4800
	ds_read_b64_tr_b16 v[154:155], v177 offset:0x5800
	s_waitcnt lgkmcnt(6)
	v_mfma_f32_32x32x16_bf16 v[64:79], v[204:207], v[140:143], v[64:79]
	ds_read_b64_tr_b16 v[156:157], v177 offset:0x6800
	ds_read_b64_tr_b16 v[158:159], v177 offset:0x7800
	s_waitcnt lgkmcnt(6)
	v_mfma_f32_32x32x16_bf16 v[48:63], v[144:147], v[128:131], v[48:63]
	ds_read_b64_tr_b16 v[192:193], v177 offset:0xa00
	ds_read_b64_tr_b16 v[194:195], v177 offset:0x1a00
	s_waitcnt lgkmcnt(6)
	v_mfma_f32_32x32x16_bf16 v[48:63], v[148:151], v[132:135], v[48:63]
	ds_read_b64_tr_b16 v[196:197], v177 offset:0x2a00
	ds_read_b64_tr_b16 v[198:199], v177 offset:0x3a00
	s_waitcnt lgkmcnt(6)
	v_mfma_f32_32x32x16_bf16 v[48:63], v[152:155], v[136:139], v[48:63]
	ds_read_b64_tr_b16 v[200:201], v177 offset:0x4a00
	ds_read_b64_tr_b16 v[202:203], v177 offset:0x5a00
	s_waitcnt lgkmcnt(6)
	v_mfma_f32_32x32x16_bf16 v[48:63], v[156:159], v[140:143], v[48:63]
	ds_read_b64_tr_b16 v[204:205], v177 offset:0x6a00
	ds_read_b64_tr_b16 v[206:207], v177 offset:0x7a00
	s_waitcnt lgkmcnt(6)
	v_mfma_f32_32x32x16_bf16 v[32:47], v[192:195], v[128:131], v[32:47]
	ds_read_b64_tr_b16 v[144:145], v177 offset:0xc00
	ds_read_b64_tr_b16 v[146:147], v177 offset:0x1c00
	s_waitcnt lgkmcnt(6)
	v_mfma_f32_32x32x16_bf16 v[32:47], v[196:199], v[132:135], v[32:47]
	ds_read_b64_tr_b16 v[148:149], v177 offset:0x2c00
	ds_read_b64_tr_b16 v[150:151], v177 offset:0x3c00
	s_waitcnt lgkmcnt(6)
	v_mfma_f32_32x32x16_bf16 v[32:47], v[200:203], v[136:139], v[32:47]
	ds_read_b64_tr_b16 v[152:153], v177 offset:0x4c00
	ds_read_b64_tr_b16 v[154:155], v177 offset:0x5c00
	s_waitcnt lgkmcnt(6)
	v_mfma_f32_32x32x16_bf16 v[32:47], v[204:207], v[140:143], v[32:47]
	ds_read_b64_tr_b16 v[156:157], v177 offset:0x6c00
	ds_read_b64_tr_b16 v[158:159], v177 offset:0x7c00
	s_waitcnt lgkmcnt(6)
	v_mfma_f32_32x32x16_bf16 v[16:31], v[144:147], v[128:131], v[16:31]
	ds_read_b64_tr_b16 v[192:193], v177 offset:0xe00
	ds_read_b64_tr_b16 v[194:195], v177 offset:0x1e00
	s_waitcnt lgkmcnt(6)
	v_mfma_f32_32x32x16_bf16 v[16:31], v[148:151], v[132:135], v[16:31]
	ds_read_b64_tr_b16 v[196:197], v177 offset:0x2e00
	ds_read_b64_tr_b16 v[198:199], v177 offset:0x3e00
	s_waitcnt lgkmcnt(6)
	v_mfma_f32_32x32x16_bf16 v[16:31], v[152:155], v[136:139], v[16:31]
	ds_read_b64_tr_b16 v[200:201], v177 offset:0x4e00
	ds_read_b64_tr_b16 v[202:203], v177 offset:0x5e00
	s_waitcnt lgkmcnt(6)
	v_mfma_f32_32x32x16_bf16 v[16:31], v[156:159], v[140:143], v[16:31]
	ds_read_b64_tr_b16 v[204:205], v177 offset:0x6e00
	ds_read_b64_tr_b16 v[206:207], v177 offset:0x7e00
	s_waitcnt lgkmcnt(6)
	v_mfma_f32_32x32x16_bf16 v[0:15], v[192:195], v[128:131], v[0:15]
	s_waitcnt lgkmcnt(4)
	v_mfma_f32_32x32x16_bf16 v[0:15], v[196:199], v[132:135], v[0:15]
	s_waitcnt lgkmcnt(2)
	v_mfma_f32_32x32x16_bf16 v[0:15], v[200:203], v[136:139], v[0:15]
	s_waitcnt lgkmcnt(0)
	v_mfma_f32_32x32x16_bf16 v[0:15], v[204:207], v[140:143], v[0:15]
	ds_read_b128 v[128:131], v188 offset:0
	ds_read_b128 v[132:135], v188 offset:0x2000
	ds_read_b128 v[192:195], v187 offset:0
	ds_read_b128 v[196:199], v187 offset:0x2000
	s_waitcnt lgkmcnt(2)
	s_nop 0
	v_mfma_f32_32x32x16_bf16 v[144:159], v[128:131], v[218:221], 0
	v_mfma_f32_32x32x16_bf16 v[128:143], v[132:135], v[218:221], 0
	ds_read_b128 v[204:207], v186 offset:0
	ds_read_b128 v[208:211], v186 offset:0x2000
	s_waitcnt lgkmcnt(2)
	v_mfma_f32_32x32x16_bf16 v[144:159], v[192:195], v[222:225], v[144:159]
	v_mfma_f32_32x32x16_bf16 v[128:143], v[196:199], v[222:225], v[128:143]
	ds_read_b128 v[192:195], v185 offset:0
	ds_read_b128 v[196:199], v185 offset:0x2000
	s_waitcnt lgkmcnt(2)
	v_mfma_f32_32x32x16_bf16 v[144:159], v[204:207], v[230:233], v[144:159]
	v_mfma_f32_32x32x16_bf16 v[128:143], v[208:211], v[230:233], v[128:143]
	ds_read_b128 v[204:207], v188 offset:0x80
	ds_read_b128 v[208:211], v188 offset:0x2080
	s_waitcnt lgkmcnt(2)
	v_mfma_f32_32x32x16_bf16 v[144:159], v[192:195], v[234:237], v[144:159]
	v_mfma_f32_32x32x16_bf16 v[128:143], v[196:199], v[234:237], v[128:143]
	ds_read_b128 v[192:195], v187 offset:0x80
	ds_read_b128 v[196:199], v187 offset:0x2080
	s_waitcnt lgkmcnt(2)
	v_mfma_f32_32x32x16_bf16 v[144:159], v[204:207], v[238:241], v[144:159]
	v_mfma_f32_32x32x16_bf16 v[128:143], v[208:211], v[238:241], v[128:143]
	ds_read_b128 v[204:207], v186 offset:0x80
	ds_read_b128 v[208:211], v186 offset:0x2080
	s_waitcnt lgkmcnt(2)
	v_mfma_f32_32x32x16_bf16 v[144:159], v[192:195], v[242:245], v[144:159]
	v_mfma_f32_32x32x16_bf16 v[128:143], v[196:199], v[242:245], v[128:143]
	ds_read_b128 v[192:195], v185 offset:0x80
	ds_read_b128 v[196:199], v185 offset:0x2080
	s_waitcnt lgkmcnt(2)
	v_mfma_f32_32x32x16_bf16 v[144:159], v[204:207], v[246:249], v[144:159]
	v_mfma_f32_32x32x16_bf16 v[128:143], v[208:211], v[246:249], v[128:143]
	s_waitcnt lgkmcnt(0)
	v_mfma_f32_32x32x16_bf16 v[144:159], v[192:195], v[166:169], v[144:159]
	v_mfma_f32_32x32x16_bf16 v[128:143], v[196:199], v[166:169], v[128:143]
	s_bitcmp0_b32 s100, 8
	s_cbranch_scc1 .Lstg_a18
	s_waitcnt vmcnt(0)
	s_waitcnt lgkmcnt(0)
	s_barrier
	s_sleep 6

.LBB0_597:
	ds_read_b64_tr_b16 v[144:145], v177 offset:0x8000
	ds_read_b64_tr_b16 v[146:147], v177 offset:0x9000
	ds_read_b64_tr_b16 v[148:149], v177 offset:0xa000
	ds_read_b64_tr_b16 v[150:151], v177 offset:0xb000
	ds_read_b64_tr_b16 v[152:153], v177 offset:0xc000
	ds_read_b64_tr_b16 v[154:155], v177 offset:0xd000
	ds_read_b64_tr_b16 v[156:157], v177 offset:0xe000
	ds_read_b64_tr_b16 v[158:159], v177 offset:0xf000
	s_waitcnt lgkmcnt(6)
	s_nop 0
	v_mfma_f32_32x32x16_bf16 v[112:127], v[144:147], v[128:131], v[112:127]
	ds_read_b64_tr_b16 v[194:195], v177 offset:0x8200
	ds_read_b64_tr_b16 v[196:197], v177 offset:0x9200
	s_waitcnt lgkmcnt(6)
	v_mfma_f32_32x32x16_bf16 v[112:127], v[148:151], v[132:135], v[112:127]
	ds_read_b64_tr_b16 v[198:199], v177 offset:0xa200
	ds_read_b64_tr_b16 v[200:201], v177 offset:0xb200
	s_waitcnt lgkmcnt(6)
	v_mfma_f32_32x32x16_bf16 v[112:127], v[152:155], v[136:139], v[112:127]
	ds_read_b64_tr_b16 v[202:203], v177 offset:0xc200
	ds_read_b64_tr_b16 v[204:205], v177 offset:0xd200
	s_waitcnt lgkmcnt(6)
	v_mfma_f32_32x32x16_bf16 v[112:127], v[156:159], v[140:143], v[112:127]
	ds_read_b64_tr_b16 v[206:207], v177 offset:0xe200
	ds_read_b64_tr_b16 v[208:209], v177 offset:0xf200
	s_waitcnt lgkmcnt(6)
	v_mfma_f32_32x32x16_bf16 v[96:111], v[194:197], v[128:131], v[96:111]
	ds_read_b64_tr_b16 v[144:145], v177 offset:0x8400
	ds_read_b64_tr_b16 v[146:147], v177 offset:0x9400
	s_waitcnt lgkmcnt(6)
	v_mfma_f32_32x32x16_bf16 v[96:111], v[198:201], v[132:135], v[96:111]
	ds_read_b64_tr_b16 v[148:149], v177 offset:0xa400
	ds_read_b64_tr_b16 v[150:151], v177 offset:0xb400
	s_waitcnt lgkmcnt(6)
	v_mfma_f32_32x32x16_bf16 v[96:111], v[202:205], v[136:139], v[96:111]
	ds_read_b64_tr_b16 v[152:153], v177 offset:0xc400
	ds_read_b64_tr_b16 v[154:155], v177 offset:0xd400
	s_waitcnt lgkmcnt(6)
	v_mfma_f32_32x32x16_bf16 v[96:111], v[206:209], v[140:143], v[96:111]
	ds_read_b64_tr_b16 v[156:157], v177 offset:0xe400
	ds_read_b64_tr_b16 v[158:159], v177 offset:0xf400
	s_waitcnt lgkmcnt(6)
	v_mfma_f32_32x32x16_bf16 v[80:95], v[144:147], v[128:131], v[80:95]
	ds_read_b64_tr_b16 v[194:195], v177 offset:0x8600
	ds_read_b64_tr_b16 v[196:197], v177 offset:0x9600
	s_waitcnt lgkmcnt(6)
	v_mfma_f32_32x32x16_bf16 v[80:95], v[148:151], v[132:135], v[80:95]
	ds_read_b64_tr_b16 v[198:199], v177 offset:0xa600
	ds_read_b64_tr_b16 v[200:201], v177 offset:0xb600
	s_waitcnt lgkmcnt(6)
	v_mfma_f32_32x32x16_bf16 v[80:95], v[152:155], v[136:139], v[80:95]
	ds_read_b64_tr_b16 v[202:203], v177 offset:0xc600
	ds_read_b64_tr_b16 v[204:205], v177 offset:0xd600
	s_waitcnt lgkmcnt(6)
	v_mfma_f32_32x32x16_bf16 v[80:95], v[156:159], v[140:143], v[80:95]
	ds_read_b64_tr_b16 v[206:207], v177 offset:0xe600
	ds_read_b64_tr_b16 v[208:209], v177 offset:0xf600
	s_waitcnt lgkmcnt(6)
	v_mfma_f32_32x32x16_bf16 v[64:79], v[194:197], v[128:131], v[64:79]
	ds_read_b64_tr_b16 v[144:145], v177 offset:0x8800
	ds_read_b64_tr_b16 v[146:147], v177 offset:0x9800
	s_waitcnt lgkmcnt(6)
	v_mfma_f32_32x32x16_bf16 v[64:79], v[198:201], v[132:135], v[64:79]
	ds_read_b64_tr_b16 v[148:149], v177 offset:0xa800
	ds_read_b64_tr_b16 v[150:151], v177 offset:0xb800
	s_waitcnt lgkmcnt(6)
	v_mfma_f32_32x32x16_bf16 v[64:79], v[202:205], v[136:139], v[64:79]
	ds_read_b64_tr_b16 v[152:153], v177 offset:0xc800
	ds_read_b64_tr_b16 v[154:155], v177 offset:0xd800
	s_waitcnt lgkmcnt(6)
	v_mfma_f32_32x32x16_bf16 v[64:79], v[206:209], v[140:143], v[64:79]
	ds_read_b64_tr_b16 v[156:157], v177 offset:0xe800
	ds_read_b64_tr_b16 v[158:159], v177 offset:0xf800
	s_waitcnt lgkmcnt(6)
	v_mfma_f32_32x32x16_bf16 v[48:63], v[144:147], v[128:131], v[48:63]
	ds_read_b64_tr_b16 v[194:195], v177 offset:0x8a00
	ds_read_b64_tr_b16 v[196:197], v177 offset:0x9a00
	s_waitcnt lgkmcnt(6)
	v_mfma_f32_32x32x16_bf16 v[48:63], v[148:151], v[132:135], v[48:63]
	ds_read_b64_tr_b16 v[198:199], v177 offset:0xaa00
	ds_read_b64_tr_b16 v[200:201], v177 offset:0xba00
	s_waitcnt lgkmcnt(6)
	v_mfma_f32_32x32x16_bf16 v[48:63], v[152:155], v[136:139], v[48:63]
	ds_read_b64_tr_b16 v[202:203], v177 offset:0xca00
	ds_read_b64_tr_b16 v[204:205], v177 offset:0xda00
	s_waitcnt lgkmcnt(6)
	v_mfma_f32_32x32x16_bf16 v[48:63], v[156:159], v[140:143], v[48:63]
	ds_read_b64_tr_b16 v[206:207], v177 offset:0xea00
	ds_read_b64_tr_b16 v[208:209], v177 offset:0xfa00
	s_waitcnt lgkmcnt(6)
	v_mfma_f32_32x32x16_bf16 v[32:47], v[194:197], v[128:131], v[32:47]
	ds_read_b64_tr_b16 v[144:145], v177 offset:0x8c00
	ds_read_b64_tr_b16 v[146:147], v177 offset:0x9c00
	s_waitcnt lgkmcnt(6)
	v_mfma_f32_32x32x16_bf16 v[32:47], v[198:201], v[132:135], v[32:47]
	ds_read_b64_tr_b16 v[148:149], v177 offset:0xac00
	ds_read_b64_tr_b16 v[150:151], v177 offset:0xbc00
	s_waitcnt lgkmcnt(6)
	v_mfma_f32_32x32x16_bf16 v[32:47], v[202:205], v[136:139], v[32:47]
	ds_read_b64_tr_b16 v[152:153], v177 offset:0xcc00
	ds_read_b64_tr_b16 v[154:155], v177 offset:0xdc00
	s_waitcnt lgkmcnt(6)
	v_mfma_f32_32x32x16_bf16 v[32:47], v[206:209], v[140:143], v[32:47]
	ds_read_b64_tr_b16 v[156:157], v177 offset:0xec00
	ds_read_b64_tr_b16 v[158:159], v177 offset:0xfc00
	s_waitcnt lgkmcnt(6)
	v_mfma_f32_32x32x16_bf16 v[16:31], v[144:147], v[128:131], v[16:31]
	ds_read_b64_tr_b16 v[194:195], v177 offset:0x8e00
	ds_read_b64_tr_b16 v[196:197], v177 offset:0x9e00
	s_waitcnt lgkmcnt(6)
	v_mfma_f32_32x32x16_bf16 v[16:31], v[148:151], v[132:135], v[16:31]
	ds_read_b64_tr_b16 v[198:199], v177 offset:0xae00
	ds_read_b64_tr_b16 v[200:201], v177 offset:0xbe00
	s_waitcnt lgkmcnt(6)
	v_mfma_f32_32x32x16_bf16 v[16:31], v[152:155], v[136:139], v[16:31]
	ds_read_b64_tr_b16 v[202:203], v177 offset:0xce00
	ds_read_b64_tr_b16 v[204:205], v177 offset:0xde00
	s_waitcnt lgkmcnt(6)
	v_mfma_f32_32x32x16_bf16 v[16:31], v[156:159], v[140:143], v[16:31]
	ds_read_b64_tr_b16 v[206:207], v177 offset:0xee00
	ds_read_b64_tr_b16 v[208:209], v177 offset:0xfe00
	s_waitcnt lgkmcnt(6)
	v_mfma_f32_32x32x16_bf16 v[0:15], v[194:197], v[128:131], v[0:15]
	s_waitcnt lgkmcnt(4)
	v_mfma_f32_32x32x16_bf16 v[0:15], v[198:201], v[132:135], v[0:15]
	s_waitcnt lgkmcnt(2)
	v_mfma_f32_32x32x16_bf16 v[0:15], v[202:205], v[136:139], v[0:15]
	s_waitcnt lgkmcnt(0)
	v_mfma_f32_32x32x16_bf16 v[0:15], v[206:209], v[140:143], v[0:15]
	ds_read_b128 v[128:131], v181 offset:0
	ds_read_b128 v[132:135], v181 offset:0x2000
	ds_read_b128 v[194:197], v182 offset:0
	ds_read_b128 v[198:201], v182 offset:0x2000
	s_waitcnt lgkmcnt(2)
	s_nop 0
	v_mfma_f32_32x32x16_bf16 v[144:159], v[128:131], v[218:221], 0
	v_mfma_f32_32x32x16_bf16 v[128:143], v[132:135], v[218:221], 0
	ds_read_b128 v[206:209], v183 offset:0
	ds_read_b128 v[210:213], v183 offset:0x2000
	s_waitcnt lgkmcnt(2)
	v_mfma_f32_32x32x16_bf16 v[144:159], v[194:197], v[222:225], v[144:159]
	v_mfma_f32_32x32x16_bf16 v[128:143], v[198:201], v[222:225], v[128:143]
	ds_read_b128 v[194:197], v184 offset:0
	ds_read_b128 v[198:201], v184 offset:0x2000
	s_waitcnt lgkmcnt(2)
	v_mfma_f32_32x32x16_bf16 v[144:159], v[206:209], v[230:233], v[144:159]
	v_mfma_f32_32x32x16_bf16 v[128:143], v[210:213], v[230:233], v[128:143]
	ds_read_b128 v[206:209], v181 offset:0x80
	ds_read_b128 v[210:213], v181 offset:0x2080
	s_waitcnt lgkmcnt(2)
	v_mfma_f32_32x32x16_bf16 v[144:159], v[194:197], v[234:237], v[144:159]
	v_mfma_f32_32x32x16_bf16 v[128:143], v[198:201], v[234:237], v[128:143]
	ds_read_b128 v[194:197], v182 offset:0x80
	ds_read_b128 v[198:201], v182 offset:0x2080
	s_waitcnt lgkmcnt(2)
	v_mfma_f32_32x32x16_bf16 v[144:159], v[206:209], v[238:241], v[144:159]
	v_mfma_f32_32x32x16_bf16 v[128:143], v[210:213], v[238:241], v[128:143]
	ds_read_b128 v[206:209], v183 offset:0x80
	ds_read_b128 v[210:213], v183 offset:0x2080
	s_waitcnt lgkmcnt(2)
	v_mfma_f32_32x32x16_bf16 v[144:159], v[194:197], v[242:245], v[144:159]
	v_mfma_f32_32x32x16_bf16 v[128:143], v[198:201], v[242:245], v[128:143]
	ds_read_b128 v[194:197], v184 offset:0x80
	ds_read_b128 v[198:201], v184 offset:0x2080
	s_waitcnt lgkmcnt(2)
	v_mfma_f32_32x32x16_bf16 v[144:159], v[206:209], v[246:249], v[144:159]
	v_mfma_f32_32x32x16_bf16 v[128:143], v[210:213], v[246:249], v[128:143]
	s_waitcnt lgkmcnt(0)
	v_mfma_f32_32x32x16_bf16 v[144:159], v[194:197], v[166:169], v[144:159]
	v_mfma_f32_32x32x16_bf16 v[128:143], v[198:201], v[166:169], v[128:143]
	s_bitcmp0_b32 s100, 8
	s_cbranch_scc1 .Lstg_a19
	s_waitcnt vmcnt(0)
	s_waitcnt lgkmcnt(0)
	s_barrier
	s_sleep 6

.LBB0_612:
	ds_read_b64_tr_b16 v[144:145], v177 offset:0
	ds_read_b64_tr_b16 v[146:147], v177 offset:0x1000
	ds_read_b64_tr_b16 v[148:149], v177 offset:0x2000
	ds_read_b64_tr_b16 v[150:151], v177 offset:0x3000
	ds_read_b64_tr_b16 v[152:153], v177 offset:0x4000
	ds_read_b64_tr_b16 v[154:155], v177 offset:0x5000
	ds_read_b64_tr_b16 v[156:157], v177 offset:0x6000
	ds_read_b64_tr_b16 v[158:159], v177 offset:0x7000
	s_waitcnt lgkmcnt(6)
	s_nop 0
	v_mfma_f32_32x32x16_bf16 v[112:127], v[144:147], v[128:131], v[112:127]
	ds_read_b64_tr_b16 v[192:193], v177 offset:0x200
	ds_read_b64_tr_b16 v[194:195], v177 offset:0x1200
	s_waitcnt lgkmcnt(6)
	v_mfma_f32_32x32x16_bf16 v[112:127], v[148:151], v[132:135], v[112:127]
	ds_read_b64_tr_b16 v[196:197], v177 offset:0x2200
	ds_read_b64_tr_b16 v[198:199], v177 offset:0x3200
	s_waitcnt lgkmcnt(6)
	v_mfma_f32_32x32x16_bf16 v[112:127], v[152:155], v[136:139], v[112:127]
	ds_read_b64_tr_b16 v[200:201], v177 offset:0x4200
	ds_read_b64_tr_b16 v[202:203], v177 offset:0x5200
	s_waitcnt lgkmcnt(6)
	v_mfma_f32_32x32x16_bf16 v[112:127], v[156:159], v[140:143], v[112:127]
	ds_read_b64_tr_b16 v[204:205], v177 offset:0x6200
	ds_read_b64_tr_b16 v[206:207], v177 offset:0x7200
	s_waitcnt lgkmcnt(6)
	v_mfma_f32_32x32x16_bf16 v[96:111], v[192:195], v[128:131], v[96:111]
	ds_read_b64_tr_b16 v[144:145], v177 offset:0x400
	ds_read_b64_tr_b16 v[146:147], v177 offset:0x1400
	s_waitcnt lgkmcnt(6)
	v_mfma_f32_32x32x16_bf16 v[96:111], v[196:199], v[132:135], v[96:111]
	ds_read_b64_tr_b16 v[148:149], v177 offset:0x2400
	ds_read_b64_tr_b16 v[150:151], v177 offset:0x3400
	s_waitcnt lgkmcnt(6)
	v_mfma_f32_32x32x16_bf16 v[96:111], v[200:203], v[136:139], v[96:111]
	ds_read_b64_tr_b16 v[152:153], v177 offset:0x4400
	ds_read_b64_tr_b16 v[154:155], v177 offset:0x5400
	s_waitcnt lgkmcnt(6)
	v_mfma_f32_32x32x16_bf16 v[96:111], v[204:207], v[140:143], v[96:111]
	ds_read_b64_tr_b16 v[156:157], v177 offset:0x6400
	ds_read_b64_tr_b16 v[158:159], v177 offset:0x7400
	s_waitcnt lgkmcnt(6)
	v_mfma_f32_32x32x16_bf16 v[80:95], v[144:147], v[128:131], v[80:95]
	ds_read_b64_tr_b16 v[192:193], v177 offset:0x600
	ds_read_b64_tr_b16 v[194:195], v177 offset:0x1600
	s_waitcnt lgkmcnt(6)
	v_mfma_f32_32x32x16_bf16 v[80:95], v[148:151], v[132:135], v[80:95]
	ds_read_b64_tr_b16 v[196:197], v177 offset:0x2600
	ds_read_b64_tr_b16 v[198:199], v177 offset:0x3600
	s_waitcnt lgkmcnt(6)
	v_mfma_f32_32x32x16_bf16 v[80:95], v[152:155], v[136:139], v[80:95]
	ds_read_b64_tr_b16 v[200:201], v177 offset:0x4600
	ds_read_b64_tr_b16 v[202:203], v177 offset:0x5600
	s_waitcnt lgkmcnt(6)
	v_mfma_f32_32x32x16_bf16 v[80:95], v[156:159], v[140:143], v[80:95]
	ds_read_b64_tr_b16 v[204:205], v177 offset:0x6600
	ds_read_b64_tr_b16 v[206:207], v177 offset:0x7600
	s_waitcnt lgkmcnt(6)
	v_mfma_f32_32x32x16_bf16 v[64:79], v[192:195], v[128:131], v[64:79]
	ds_read_b64_tr_b16 v[144:145], v177 offset:0x800
	ds_read_b64_tr_b16 v[146:147], v177 offset:0x1800
	s_waitcnt lgkmcnt(6)
	v_mfma_f32_32x32x16_bf16 v[64:79], v[196:199], v[132:135], v[64:79]
	ds_read_b64_tr_b16 v[148:149], v177 offset:0x2800
	ds_read_b64_tr_b16 v[150:151], v177 offset:0x3800
	s_waitcnt lgkmcnt(6)
	v_mfma_f32_32x32x16_bf16 v[64:79], v[200:203], v[136:139], v[64:79]
	ds_read_b64_tr_b16 v[152:153], v177 offset:0x4800
	ds_read_b64_tr_b16 v[154:155], v177 offset:0x5800
	s_waitcnt lgkmcnt(6)
	v_mfma_f32_32x32x16_bf16 v[64:79], v[204:207], v[140:143], v[64:79]
	ds_read_b64_tr_b16 v[156:157], v177 offset:0x6800
	ds_read_b64_tr_b16 v[158:159], v177 offset:0x7800
	s_waitcnt lgkmcnt(6)
	v_mfma_f32_32x32x16_bf16 v[48:63], v[144:147], v[128:131], v[48:63]
	ds_read_b64_tr_b16 v[192:193], v177 offset:0xa00
	ds_read_b64_tr_b16 v[194:195], v177 offset:0x1a00
	s_waitcnt lgkmcnt(6)
	v_mfma_f32_32x32x16_bf16 v[48:63], v[148:151], v[132:135], v[48:63]
	ds_read_b64_tr_b16 v[196:197], v177 offset:0x2a00
	ds_read_b64_tr_b16 v[198:199], v177 offset:0x3a00
	s_waitcnt lgkmcnt(6)
	v_mfma_f32_32x32x16_bf16 v[48:63], v[152:155], v[136:139], v[48:63]
	ds_read_b64_tr_b16 v[200:201], v177 offset:0x4a00
	ds_read_b64_tr_b16 v[202:203], v177 offset:0x5a00
	s_waitcnt lgkmcnt(6)
	v_mfma_f32_32x32x16_bf16 v[48:63], v[156:159], v[140:143], v[48:63]
	ds_read_b64_tr_b16 v[204:205], v177 offset:0x6a00
	ds_read_b64_tr_b16 v[206:207], v177 offset:0x7a00
	s_waitcnt lgkmcnt(6)
	v_mfma_f32_32x32x16_bf16 v[32:47], v[192:195], v[128:131], v[32:47]
	ds_read_b64_tr_b16 v[144:145], v177 offset:0xc00
	ds_read_b64_tr_b16 v[146:147], v177 offset:0x1c00
	s_waitcnt lgkmcnt(6)
	v_mfma_f32_32x32x16_bf16 v[32:47], v[196:199], v[132:135], v[32:47]
	ds_read_b64_tr_b16 v[148:149], v177 offset:0x2c00
	ds_read_b64_tr_b16 v[150:151], v177 offset:0x3c00
	s_waitcnt lgkmcnt(6)
	v_mfma_f32_32x32x16_bf16 v[32:47], v[200:203], v[136:139], v[32:47]
	ds_read_b64_tr_b16 v[152:153], v177 offset:0x4c00
	ds_read_b64_tr_b16 v[154:155], v177 offset:0x5c00
	s_waitcnt lgkmcnt(6)
	v_mfma_f32_32x32x16_bf16 v[32:47], v[204:207], v[140:143], v[32:47]
	ds_read_b64_tr_b16 v[156:157], v177 offset:0x6c00
	ds_read_b64_tr_b16 v[158:159], v177 offset:0x7c00
	s_waitcnt lgkmcnt(6)
	v_mfma_f32_32x32x16_bf16 v[16:31], v[144:147], v[128:131], v[16:31]
	ds_read_b64_tr_b16 v[192:193], v177 offset:0xe00
	ds_read_b64_tr_b16 v[194:195], v177 offset:0x1e00
	s_waitcnt lgkmcnt(6)
	v_mfma_f32_32x32x16_bf16 v[16:31], v[148:151], v[132:135], v[16:31]
	ds_read_b64_tr_b16 v[196:197], v177 offset:0x2e00
	ds_read_b64_tr_b16 v[198:199], v177 offset:0x3e00
	s_waitcnt lgkmcnt(6)
	v_mfma_f32_32x32x16_bf16 v[16:31], v[152:155], v[136:139], v[16:31]
	ds_read_b64_tr_b16 v[200:201], v177 offset:0x4e00
	ds_read_b64_tr_b16 v[202:203], v177 offset:0x5e00
	s_waitcnt lgkmcnt(6)
	v_mfma_f32_32x32x16_bf16 v[16:31], v[156:159], v[140:143], v[16:31]
	ds_read_b64_tr_b16 v[204:205], v177 offset:0x6e00
	ds_read_b64_tr_b16 v[206:207], v177 offset:0x7e00
	s_waitcnt lgkmcnt(6)
	v_mfma_f32_32x32x16_bf16 v[0:15], v[192:195], v[128:131], v[0:15]
	s_waitcnt lgkmcnt(4)
	v_mfma_f32_32x32x16_bf16 v[0:15], v[196:199], v[132:135], v[0:15]
	s_waitcnt lgkmcnt(2)
	v_mfma_f32_32x32x16_bf16 v[0:15], v[200:203], v[136:139], v[0:15]
	s_waitcnt lgkmcnt(0)
	v_mfma_f32_32x32x16_bf16 v[0:15], v[204:207], v[140:143], v[0:15]
	ds_read_b128 v[128:131], v188 offset:0
	ds_read_b128 v[132:135], v188 offset:0x2000
	ds_read_b128 v[192:195], v187 offset:0
	ds_read_b128 v[196:199], v187 offset:0x2000
	s_waitcnt lgkmcnt(2)
	s_nop 0
	v_mfma_f32_32x32x16_bf16 v[144:159], v[128:131], v[218:221], 0
	v_mfma_f32_32x32x16_bf16 v[128:143], v[132:135], v[218:221], 0
	ds_read_b128 v[204:207], v186 offset:0
	ds_read_b128 v[208:211], v186 offset:0x2000
	s_waitcnt lgkmcnt(2)
	v_mfma_f32_32x32x16_bf16 v[144:159], v[192:195], v[222:225], v[144:159]
	v_mfma_f32_32x32x16_bf16 v[128:143], v[196:199], v[222:225], v[128:143]
	ds_read_b128 v[192:195], v185 offset:0
	ds_read_b128 v[196:199], v185 offset:0x2000
	s_waitcnt lgkmcnt(2)
	v_mfma_f32_32x32x16_bf16 v[144:159], v[204:207], v[230:233], v[144:159]
	v_mfma_f32_32x32x16_bf16 v[128:143], v[208:211], v[230:233], v[128:143]
	ds_read_b128 v[204:207], v188 offset:0x80
	ds_read_b128 v[208:211], v188 offset:0x2080
	s_waitcnt lgkmcnt(2)
	v_mfma_f32_32x32x16_bf16 v[144:159], v[192:195], v[234:237], v[144:159]
	v_mfma_f32_32x32x16_bf16 v[128:143], v[196:199], v[234:237], v[128:143]
	ds_read_b128 v[192:195], v187 offset:0x80
	ds_read_b128 v[196:199], v187 offset:0x2080
	s_waitcnt lgkmcnt(2)
	v_mfma_f32_32x32x16_bf16 v[144:159], v[204:207], v[238:241], v[144:159]
	v_mfma_f32_32x32x16_bf16 v[128:143], v[208:211], v[238:241], v[128:143]
	ds_read_b128 v[204:207], v186 offset:0x80
	ds_read_b128 v[208:211], v186 offset:0x2080
	s_waitcnt lgkmcnt(2)
	v_mfma_f32_32x32x16_bf16 v[144:159], v[192:195], v[242:245], v[144:159]
	v_mfma_f32_32x32x16_bf16 v[128:143], v[196:199], v[242:245], v[128:143]
	ds_read_b128 v[180:183], v185 offset:0x80
	ds_read_b128 v[192:195], v185 offset:0x2080
	s_waitcnt lgkmcnt(2)
	v_mfma_f32_32x32x16_bf16 v[144:159], v[204:207], v[246:249], v[144:159]
	v_mfma_f32_32x32x16_bf16 v[128:143], v[208:211], v[246:249], v[128:143]
	s_waitcnt lgkmcnt(0)
	v_mfma_f32_32x32x16_bf16 v[144:159], v[180:183], v[166:169], v[144:159]
	v_mfma_f32_32x32x16_bf16 v[128:143], v[192:195], v[166:169], v[128:143]
	s_bitcmp0_b32 s100, 8
	s_cbranch_scc1 .Lstg_a20
	s_waitcnt vmcnt(0)
	s_waitcnt lgkmcnt(0)
	s_barrier
	s_sleep 6
